# GEMM epilogue output stores (in-proj, up, down) marked nt; on top of v26
# baseline (speedup 1.0000x reference)
; __device__ __forceinline__ unsigned cvt_pk_bf16(float lo, float hi) { unsigned r; asm volatile("v_cvt_pk_bf16_f32 %0, %1, %2" : "=v"(r) : "v"(lo), "v"(hi)); return r; }
;     __device__ __forceinline__ void operator()(const f32x4 (&acc)[2][2][4][2], const Unit& u, int wr, int wc, int fr, int fq) const {
;         const int row0 = u.pm * BM + wr * 64 + fr; const int pn = u.pn;
;         if (pn < 16) {
;             bf16_t* base = (pn < 8) ? Q : K; const int hp = (pn & 7) * 2; const float sgn = (fq >= 2) ? 1.0f : -1.0f;
; #pragma unroll
;             for (int ai = 0; ai < 2; ++ai)
; #pragma unroll
;                 for (int m = 0; m < 4; ++m) { const int row = row0 + ai * HALF + m * 16;
;                     f32x4 cs0 = (f32x4){1.f, 1.f, 1.f, 1.f}, cs1 = cs0, sn0 = (f32x4){0.f, 0.f, 0.f, 0.f}, sn1 = sn0;
;                     if (wc == 0) { const float* rp = rope + (size_t)row * 32 + 8 * (fq & 1); cs0 = *(const f32x4*)rp; cs1 = *(const f32x4*)(rp + 4); sn0 = *(const f32x4*)(rp + 16) * sgn; sn1 = *(const f32x4*)(rp + 20) * sgn; }
; #pragma unroll
;                     for (int bj = 0; bj < 2; ++bj) { f32x4 v0 = acc[ai][bj][m][0], v1 = acc[ai][bj][m][1];
;                         if (wc == 0) { f32x4 p0, p1;
; #pragma unroll
;                             for (int i = 0; i < 4; ++i) { p0[i] = __shfl_xor(v0[i], 32); p1[i] = __shfl_xor(v1[i], 32); }
;                             v0 = v0 * cs0 + p0 * sn0; v1 = v1 * cs1 + p1 * sn1; }
;                         u32x4 w; w.x = cvt_pk_bf16(v0[0], v0[1]); w.y = cvt_pk_bf16(v0[2], v0[3]); w.z = cvt_pk_bf16(v1[0], v1[1]); w.w = cvt_pk_bf16(v1[2], v1[3]);
;                         *(u32x4*)(base + ((size_t)(hp + bj) * T_ROWS + row) * 128 + wc * 32 + 8 * fq) = w; } }
.LBB0_211:
	s_cmp_lt_i32 s50, 8
	s_cselect_b32 s4, s73, 0x3a000000
	s_lshl_b32 s6, s50, 14
	s_and_b32 s6, s6, 0x1c000
	s_mov_b32 s5, s7
	v_cvt_pk_bf16_f32 v124, v124, v125
	v_cvt_pk_bf16_f32 v125, v126, v127
	v_cvt_pk_bf16_f32 v126, v120, v121
	v_lshl_add_u64 v[120:121], v[160:161], 0, s[6:7]
	v_lshl_add_u64 v[162:163], v[150:151], 0, s[4:5]
	v_lshlrev_b64 v[120:121], 8, v[120:121]
	v_lshl_add_u64 v[120:121], v[162:163], 0, v[120:121]
	s_and_b64 vcc, exec, s[2:3]
	v_cvt_pk_bf16_f32 v127, v122, v123
	global_store_dwordx4 v[120:121], v[124:127], off nt
	s_cbranch_vccnz .LBB0_213
	v_and_b32_e32 v121, 64, v178
	v_xor_b32_e32 v120, 32, v178
	v_add_u32_e32 v121, 64, v121
	v_cmp_lt_i32_e32 vcc, v120, v121
	s_nop 1
	v_cndmask_b32_e32 v120, v178, v120, vcc
	v_lshlrev_b32_e32 v127, 2, v120
	ds_bpermute_b32 v120, v127, v116
	ds_bpermute_b32 v121, v127, v117
	ds_bpermute_b32 v122, v127, v112
	ds_bpermute_b32 v124, v127, v118
	ds_bpermute_b32 v125, v127, v119
	ds_bpermute_b32 v123, v127, v113
	ds_bpermute_b32 v126, v127, v114
	ds_bpermute_b32 v127, v127, v115
	s_waitcnt lgkmcnt(0)
	v_pk_mul_f32 v[120:121], v[170:171], v[120:121]
	v_pk_mul_f32 v[124:125], v[168:169], v[124:125]
	v_pk_fma_f32 v[116:117], v[116:117], v[132:133], v[120:121]
	v_pk_mul_f32 v[120:121], v[166:167], v[122:123]
	v_pk_mul_f32 v[122:123], v[164:165], v[126:127]
	v_pk_fma_f32 v[118:119], v[118:119], v[134:135], v[124:125]
	v_pk_fma_f32 v[114:115], v[114:115], v[130:131], v[122:123]
	v_pk_fma_f32 v[112:113], v[112:113], v[128:129], v[120:121]
.LBB0_213:
	s_or_b32 s50, s6, 0x2000
	s_mov_b32 s51, s7
	v_cvt_pk_bf16_f32 v116, v116, v117
	v_cvt_pk_bf16_f32 v117, v118, v119
	v_cvt_pk_bf16_f32 v118, v112, v113
	v_lshl_add_u64 v[112:113], v[160:161], 0, s[50:51]
	v_lshlrev_b64 v[112:113], 8, v[112:113]
	v_or_b32_e32 v120, 16, v160
	v_lshl_add_u64 v[112:113], v[162:163], 0, v[112:113]
	s_and_b64 vcc, exec, s[2:3]
	v_ashrrev_i32_e32 v121, 31, v120
	v_cvt_pk_bf16_f32 v119, v114, v115
	global_store_dwordx4 v[112:113], v[116:119], off nt
	s_cbranch_vccz .LBB0_259
	v_mov_b32_e32 v112, 1.0
	v_mov_b32_e32 v124, 0
	v_mov_b32_e32 v125, v124
	v_mov_b32_e32 v122, v124
	v_mov_b32_e32 v123, v124
	v_mov_b32_e32 v128, v124
	v_mov_b32_e32 v129, v124
	v_mov_b32_e32 v126, v124
	v_mov_b32_e32 v127, v124
	v_mov_b32_e32 v113, v112
	v_mov_b32_e32 v114, v112
	v_mov_b32_e32 v115, v112
	v_mov_b32_e32 v116, v112
	v_mov_b32_e32 v117, v112
	v_mov_b32_e32 v118, v112
	v_mov_b32_e32 v119, v112
	s_and_b64 vcc, exec, s[2:3]
	s_cbranch_vccnz .LBB0_216

; __device__ __forceinline__ unsigned cvt_pk_bf16(float lo, float hi) { unsigned r; asm volatile("v_cvt_pk_bf16_f32 %0, %1, %2" : "=v"(r) : "v"(lo), "v"(hi)); return r; }
;     __device__ __forceinline__ void operator()(const f32x4 (&acc)[2][2][4][2], const Unit& u, int wr, int wc, int fr, int fq) const {
;     ...
;                 for (int m = 0; m < 4; ++m) { const int row = row0 + ai * HALF + m * 16;
;                     f32x4 cs0 = (f32x4){1.f, 1.f, 1.f, 1.f}, cs1 = cs0, sn0 = (f32x4){0.f, 0.f, 0.f, 0.f}, sn1 = sn0;
;                     if (wc == 0) { const float* rp = rope + (size_t)row * 32 + 8 * (fq & 1); cs0 = *(const f32x4*)rp; cs1 = *(const f32x4*)(rp + 4); sn0 = *(const f32x4*)(rp + 16) * sgn; sn1 = *(const f32x4*)(rp + 20) * sgn; }
; #pragma unroll
;                     for (int bj = 0; bj < 2; ++bj) { f32x4 v0 = acc[ai][bj][m][0], v1 = acc[ai][bj][m][1];
;                         if (wc == 0) { f32x4 p0, p1;
; #pragma unroll
;                             for (int i = 0; i < 4; ++i) { p0[i] = __shfl_xor(v0[i], 32); p1[i] = __shfl_xor(v1[i], 32); }
;                             v0 = v0 * cs0 + p0 * sn0; v1 = v1 * cs1 + p1 * sn1; }
;                         u32x4 w; w.x = cvt_pk_bf16(v0[0], v0[1]); w.y = cvt_pk_bf16(v0[2], v0[3]); w.z = cvt_pk_bf16(v1[0], v1[1]); w.w = cvt_pk_bf16(v1[2], v1[3]);
;                         *(u32x4*)(base + ((size_t)(hp + bj) * T_ROWS + row) * 128 + wc * 32 + 8 * fq) = w; } }
.LBB0_216:
	v_cvt_pk_bf16_f32 v108, v108, v109
	v_cvt_pk_bf16_f32 v109, v110, v111
	s_nop 0
	v_cvt_pk_bf16_f32 v110, v104, v105
	v_lshl_add_u64 v[104:105], v[120:121], 0, s[6:7]
	v_lshlrev_b64 v[104:105], 8, v[104:105]
	v_lshl_add_u64 v[104:105], v[162:163], 0, v[104:105]
	s_and_b64 vcc, exec, s[2:3]
	v_cvt_pk_bf16_f32 v111, v106, v107
	global_store_dwordx4 v[104:105], v[108:111], off nt
	s_cbranch_vccnz .LBB0_218
	v_and_b32_e32 v105, 64, v178
	v_xor_b32_e32 v104, 32, v178
	v_add_u32_e32 v105, 64, v105
	v_cmp_lt_i32_e32 vcc, v104, v105
	s_nop 1
	v_cndmask_b32_e32 v104, v178, v104, vcc
	v_lshlrev_b32_e32 v111, 2, v104
	ds_bpermute_b32 v104, v111, v100
	ds_bpermute_b32 v105, v111, v101
	ds_bpermute_b32 v106, v111, v96
	ds_bpermute_b32 v108, v111, v102
	ds_bpermute_b32 v109, v111, v103
	ds_bpermute_b32 v107, v111, v97
	ds_bpermute_b32 v110, v111, v98
	ds_bpermute_b32 v111, v111, v99
	s_waitcnt lgkmcnt(0)
	v_pk_mul_f32 v[104:105], v[128:129], v[104:105]
	v_pk_mul_f32 v[108:109], v[126:127], v[108:109]
	v_pk_fma_f32 v[100:101], v[100:101], v[116:117], v[104:105]
	v_pk_mul_f32 v[104:105], v[124:125], v[106:107]
	v_pk_mul_f32 v[106:107], v[122:123], v[110:111]
	v_pk_fma_f32 v[102:103], v[102:103], v[118:119], v[108:109]
	v_pk_fma_f32 v[98:99], v[98:99], v[114:115], v[106:107]
	v_pk_fma_f32 v[96:97], v[96:97], v[112:113], v[104:105]
.LBB0_218:
	v_cvt_pk_bf16_f32 v100, v100, v101
	v_cvt_pk_bf16_f32 v101, v102, v103
	s_nop 0
	v_cvt_pk_bf16_f32 v102, v96, v97
	v_lshl_add_u64 v[96:97], v[120:121], 0, s[50:51]
	v_lshlrev_b64 v[96:97], 8, v[96:97]
	v_or_b32_e32 v104, 32, v160
	v_lshl_add_u64 v[96:97], v[162:163], 0, v[96:97]
	s_and_b64 vcc, exec, s[2:3]
	v_ashrrev_i32_e32 v105, 31, v104
	v_cvt_pk_bf16_f32 v103, v98, v99
	global_store_dwordx4 v[96:97], v[100:103], off nt
	s_cbranch_vccz .LBB0_260
	v_mov_b32_e32 v96, 1.0
	v_mov_b32_e32 v108, 0
	v_mov_b32_e32 v109, v108
	v_mov_b32_e32 v106, v108
	v_mov_b32_e32 v107, v108
	v_mov_b32_e32 v112, v108
	v_mov_b32_e32 v113, v108
	v_mov_b32_e32 v110, v108
	v_mov_b32_e32 v111, v108
	v_mov_b32_e32 v97, v96
	v_mov_b32_e32 v98, v96
	v_mov_b32_e32 v99, v96
	v_mov_b32_e32 v100, v96
	v_mov_b32_e32 v101, v96
	v_mov_b32_e32 v102, v96
	v_mov_b32_e32 v103, v96
	s_and_b64 vcc, exec, s[2:3]
	s_cbranch_vccnz .LBB0_221

; __device__ __forceinline__ unsigned cvt_pk_bf16(float lo, float hi) { unsigned r; asm volatile("v_cvt_pk_bf16_f32 %0, %1, %2" : "=v"(r) : "v"(lo), "v"(hi)); return r; }
;     __device__ __forceinline__ void operator()(const f32x4 (&acc)[2][2][4][2], const Unit& u, int wr, int wc, int fr, int fq) const {
;     ...
;                 for (int m = 0; m < 4; ++m) { const int row = row0 + ai * HALF + m * 16;
;                     f32x4 cs0 = (f32x4){1.f, 1.f, 1.f, 1.f}, cs1 = cs0, sn0 = (f32x4){0.f, 0.f, 0.f, 0.f}, sn1 = sn0;
;                     if (wc == 0) { const float* rp = rope + (size_t)row * 32 + 8 * (fq & 1); cs0 = *(const f32x4*)rp; cs1 = *(const f32x4*)(rp + 4); sn0 = *(const f32x4*)(rp + 16) * sgn; sn1 = *(const f32x4*)(rp + 20) * sgn; }
; #pragma unroll
;                     for (int bj = 0; bj < 2; ++bj) { f32x4 v0 = acc[ai][bj][m][0], v1 = acc[ai][bj][m][1];
;                         if (wc == 0) { f32x4 p0, p1;
; #pragma unroll
;                             for (int i = 0; i < 4; ++i) { p0[i] = __shfl_xor(v0[i], 32); p1[i] = __shfl_xor(v1[i], 32); }
;                             v0 = v0 * cs0 + p0 * sn0; v1 = v1 * cs1 + p1 * sn1; }
;                         u32x4 w; w.x = cvt_pk_bf16(v0[0], v0[1]); w.y = cvt_pk_bf16(v0[2], v0[3]); w.z = cvt_pk_bf16(v1[0], v1[1]); w.w = cvt_pk_bf16(v1[2], v1[3]);
;                         *(u32x4*)(base + ((size_t)(hp + bj) * T_ROWS + row) * 128 + wc * 32 + 8 * fq) = w; } }
.LBB0_221:
	v_cvt_pk_bf16_f32 v92, v92, v93
	v_cvt_pk_bf16_f32 v93, v94, v95
	s_nop 0
	v_cvt_pk_bf16_f32 v94, v88, v89
	v_lshl_add_u64 v[88:89], v[104:105], 0, s[6:7]
	v_lshlrev_b64 v[88:89], 8, v[88:89]
	v_lshl_add_u64 v[88:89], v[162:163], 0, v[88:89]
	s_and_b64 vcc, exec, s[2:3]
	v_cvt_pk_bf16_f32 v95, v90, v91
	global_store_dwordx4 v[88:89], v[92:95], off nt
	s_cbranch_vccnz .LBB0_223
	v_and_b32_e32 v89, 64, v178
	v_xor_b32_e32 v88, 32, v178
	v_add_u32_e32 v89, 64, v89
	v_cmp_lt_i32_e32 vcc, v88, v89
	s_nop 1
	v_cndmask_b32_e32 v88, v178, v88, vcc
	v_lshlrev_b32_e32 v95, 2, v88
	ds_bpermute_b32 v88, v95, v84
	ds_bpermute_b32 v89, v95, v85
	ds_bpermute_b32 v90, v95, v80
	ds_bpermute_b32 v92, v95, v86
	ds_bpermute_b32 v93, v95, v87
	ds_bpermute_b32 v91, v95, v81
	ds_bpermute_b32 v94, v95, v82
	ds_bpermute_b32 v95, v95, v83
	s_waitcnt lgkmcnt(0)
	v_pk_mul_f32 v[88:89], v[112:113], v[88:89]
	v_pk_mul_f32 v[92:93], v[110:111], v[92:93]
	v_pk_fma_f32 v[84:85], v[84:85], v[100:101], v[88:89]
	v_pk_mul_f32 v[88:89], v[108:109], v[90:91]
	v_pk_mul_f32 v[90:91], v[106:107], v[94:95]
	v_pk_fma_f32 v[86:87], v[86:87], v[102:103], v[92:93]
	v_pk_fma_f32 v[82:83], v[82:83], v[98:99], v[90:91]
	v_pk_fma_f32 v[80:81], v[80:81], v[96:97], v[88:89]
.LBB0_223:
	v_cvt_pk_bf16_f32 v84, v84, v85
	v_cvt_pk_bf16_f32 v85, v86, v87
	s_nop 0
	v_cvt_pk_bf16_f32 v86, v80, v81
	v_lshl_add_u64 v[80:81], v[104:105], 0, s[50:51]
	v_lshlrev_b64 v[80:81], 8, v[80:81]
	v_or_b32_e32 v88, 48, v160
	v_lshl_add_u64 v[80:81], v[162:163], 0, v[80:81]
	s_and_b64 vcc, exec, s[2:3]
	v_ashrrev_i32_e32 v89, 31, v88
	v_cvt_pk_bf16_f32 v87, v82, v83
	global_store_dwordx4 v[80:81], v[84:87], off nt
	s_cbranch_vccz .LBB0_261
	v_mov_b32_e32 v80, 1.0
	v_mov_b32_e32 v92, 0
	v_mov_b32_e32 v93, v92
	v_mov_b32_e32 v90, v92
	v_mov_b32_e32 v91, v92
	v_mov_b32_e32 v96, v92
	v_mov_b32_e32 v97, v92
	v_mov_b32_e32 v94, v92
	v_mov_b32_e32 v95, v92
	v_mov_b32_e32 v81, v80
	v_mov_b32_e32 v82, v80
	v_mov_b32_e32 v83, v80
	v_mov_b32_e32 v84, v80
	v_mov_b32_e32 v85, v80
	v_mov_b32_e32 v86, v80
	v_mov_b32_e32 v87, v80
	s_and_b64 vcc, exec, s[2:3]
	s_cbranch_vccnz .LBB0_226

; __device__ __forceinline__ unsigned cvt_pk_bf16(float lo, float hi) { unsigned r; asm volatile("v_cvt_pk_bf16_f32 %0, %1, %2" : "=v"(r) : "v"(lo), "v"(hi)); return r; }
;     __device__ __forceinline__ void operator()(const f32x4 (&acc)[2][2][4][2], const Unit& u, int wr, int wc, int fr, int fq) const {
;     ...
;                 for (int m = 0; m < 4; ++m) { const int row = row0 + ai * HALF + m * 16;
;                     f32x4 cs0 = (f32x4){1.f, 1.f, 1.f, 1.f}, cs1 = cs0, sn0 = (f32x4){0.f, 0.f, 0.f, 0.f}, sn1 = sn0;
;                     if (wc == 0) { const float* rp = rope + (size_t)row * 32 + 8 * (fq & 1); cs0 = *(const f32x4*)rp; cs1 = *(const f32x4*)(rp + 4); sn0 = *(const f32x4*)(rp + 16) * sgn; sn1 = *(const f32x4*)(rp + 20) * sgn; }
; #pragma unroll
;                     for (int bj = 0; bj < 2; ++bj) { f32x4 v0 = acc[ai][bj][m][0], v1 = acc[ai][bj][m][1];
;                         if (wc == 0) { f32x4 p0, p1;
; #pragma unroll
;                             for (int i = 0; i < 4; ++i) { p0[i] = __shfl_xor(v0[i], 32); p1[i] = __shfl_xor(v1[i], 32); }
;                             v0 = v0 * cs0 + p0 * sn0; v1 = v1 * cs1 + p1 * sn1; }
;                         u32x4 w; w.x = cvt_pk_bf16(v0[0], v0[1]); w.y = cvt_pk_bf16(v0[2], v0[3]); w.z = cvt_pk_bf16(v1[0], v1[1]); w.w = cvt_pk_bf16(v1[2], v1[3]);
;                         *(u32x4*)(base + ((size_t)(hp + bj) * T_ROWS + row) * 128 + wc * 32 + 8 * fq) = w; } }
.LBB0_226:
	v_cvt_pk_bf16_f32 v76, v76, v77
	v_cvt_pk_bf16_f32 v77, v78, v79
	s_nop 0
	v_cvt_pk_bf16_f32 v78, v72, v73
	v_lshl_add_u64 v[72:73], v[88:89], 0, s[6:7]
	v_lshlrev_b64 v[72:73], 8, v[72:73]
	v_lshl_add_u64 v[72:73], v[162:163], 0, v[72:73]
	s_and_b64 vcc, exec, s[2:3]
	v_cvt_pk_bf16_f32 v79, v74, v75
	global_store_dwordx4 v[72:73], v[76:79], off nt
	s_cbranch_vccnz .LBB0_228
	v_and_b32_e32 v73, 64, v178
	v_xor_b32_e32 v72, 32, v178
	v_add_u32_e32 v73, 64, v73
	v_cmp_lt_i32_e32 vcc, v72, v73
	s_nop 1
	v_cndmask_b32_e32 v72, v178, v72, vcc
	v_lshlrev_b32_e32 v79, 2, v72
	ds_bpermute_b32 v72, v79, v68
	ds_bpermute_b32 v73, v79, v69
	ds_bpermute_b32 v74, v79, v64
	ds_bpermute_b32 v76, v79, v70
	ds_bpermute_b32 v77, v79, v71
	ds_bpermute_b32 v75, v79, v65
	ds_bpermute_b32 v78, v79, v66
	ds_bpermute_b32 v79, v79, v67
	s_waitcnt lgkmcnt(0)
	v_pk_mul_f32 v[72:73], v[96:97], v[72:73]
	v_pk_mul_f32 v[76:77], v[94:95], v[76:77]
	v_pk_fma_f32 v[68:69], v[68:69], v[84:85], v[72:73]
	v_pk_mul_f32 v[72:73], v[92:93], v[74:75]
	v_pk_mul_f32 v[74:75], v[90:91], v[78:79]
	v_pk_fma_f32 v[70:71], v[70:71], v[86:87], v[76:77]
	v_pk_fma_f32 v[66:67], v[66:67], v[82:83], v[74:75]
	v_pk_fma_f32 v[64:65], v[64:65], v[80:81], v[72:73]
.LBB0_228:
	v_cvt_pk_bf16_f32 v68, v68, v69
	v_cvt_pk_bf16_f32 v69, v70, v71
	s_nop 0
	v_cvt_pk_bf16_f32 v70, v64, v65
	v_lshl_add_u64 v[64:65], v[88:89], 0, s[50:51]
	v_lshlrev_b64 v[64:65], 8, v[64:65]
	v_add_u32_e32 v72, 0x80, v160
	v_lshl_add_u64 v[64:65], v[162:163], 0, v[64:65]
	s_and_b64 vcc, exec, s[2:3]
	v_ashrrev_i32_e32 v73, 31, v72
	v_cvt_pk_bf16_f32 v71, v66, v67
	global_store_dwordx4 v[64:65], v[68:71], off nt
	s_cbranch_vccz .LBB0_262
	v_mov_b32_e32 v64, 1.0
	v_mov_b32_e32 v76, 0
	v_mov_b32_e32 v77, v76
	v_mov_b32_e32 v74, v76
	v_mov_b32_e32 v75, v76
	v_mov_b32_e32 v80, v76
	v_mov_b32_e32 v81, v76
	v_mov_b32_e32 v78, v76
	v_mov_b32_e32 v79, v76
	v_mov_b32_e32 v65, v64
	v_mov_b32_e32 v66, v64
	v_mov_b32_e32 v67, v64
	v_mov_b32_e32 v68, v64
	v_mov_b32_e32 v69, v64
	v_mov_b32_e32 v70, v64
	v_mov_b32_e32 v71, v64
	s_and_b64 vcc, exec, s[2:3]
	s_cbranch_vccnz .LBB0_231

; __device__ __forceinline__ unsigned cvt_pk_bf16(float lo, float hi) { unsigned r; asm volatile("v_cvt_pk_bf16_f32 %0, %1, %2" : "=v"(r) : "v"(lo), "v"(hi)); return r; }
;     __device__ __forceinline__ void operator()(const f32x4 (&acc)[2][2][4][2], const Unit& u, int wr, int wc, int fr, int fq) const {
;     ...
;                 for (int m = 0; m < 4; ++m) { const int row = row0 + ai * HALF + m * 16;
;                     f32x4 cs0 = (f32x4){1.f, 1.f, 1.f, 1.f}, cs1 = cs0, sn0 = (f32x4){0.f, 0.f, 0.f, 0.f}, sn1 = sn0;
;                     if (wc == 0) { const float* rp = rope + (size_t)row * 32 + 8 * (fq & 1); cs0 = *(const f32x4*)rp; cs1 = *(const f32x4*)(rp + 4); sn0 = *(const f32x4*)(rp + 16) * sgn; sn1 = *(const f32x4*)(rp + 20) * sgn; }
; #pragma unroll
;                     for (int bj = 0; bj < 2; ++bj) { f32x4 v0 = acc[ai][bj][m][0], v1 = acc[ai][bj][m][1];
;                         if (wc == 0) { f32x4 p0, p1;
; #pragma unroll
;                             for (int i = 0; i < 4; ++i) { p0[i] = __shfl_xor(v0[i], 32); p1[i] = __shfl_xor(v1[i], 32); }
;                             v0 = v0 * cs0 + p0 * sn0; v1 = v1 * cs1 + p1 * sn1; }
;                         u32x4 w; w.x = cvt_pk_bf16(v0[0], v0[1]); w.y = cvt_pk_bf16(v0[2], v0[3]); w.z = cvt_pk_bf16(v1[0], v1[1]); w.w = cvt_pk_bf16(v1[2], v1[3]);
;                         *(u32x4*)(base + ((size_t)(hp + bj) * T_ROWS + row) * 128 + wc * 32 + 8 * fq) = w; } }
.LBB0_231:
	v_cvt_pk_bf16_f32 v60, v60, v61
	v_cvt_pk_bf16_f32 v61, v62, v63
	s_nop 0
	v_cvt_pk_bf16_f32 v62, v56, v57
	v_lshl_add_u64 v[56:57], v[72:73], 0, s[6:7]
	v_lshlrev_b64 v[56:57], 8, v[56:57]
	v_lshl_add_u64 v[56:57], v[162:163], 0, v[56:57]
	s_and_b64 vcc, exec, s[2:3]
	v_cvt_pk_bf16_f32 v63, v58, v59
	global_store_dwordx4 v[56:57], v[60:63], off nt
	s_cbranch_vccnz .LBB0_233
	v_and_b32_e32 v57, 64, v178
	v_xor_b32_e32 v56, 32, v178
	v_add_u32_e32 v57, 64, v57
	v_cmp_lt_i32_e32 vcc, v56, v57
	s_nop 1
	v_cndmask_b32_e32 v56, v178, v56, vcc
	v_lshlrev_b32_e32 v63, 2, v56
	ds_bpermute_b32 v56, v63, v52
	ds_bpermute_b32 v57, v63, v53
	ds_bpermute_b32 v58, v63, v48
	ds_bpermute_b32 v60, v63, v54
	ds_bpermute_b32 v61, v63, v55
	ds_bpermute_b32 v59, v63, v49
	ds_bpermute_b32 v62, v63, v50
	ds_bpermute_b32 v63, v63, v51
	s_waitcnt lgkmcnt(0)
	v_pk_mul_f32 v[56:57], v[80:81], v[56:57]
	v_pk_mul_f32 v[60:61], v[78:79], v[60:61]
	v_pk_fma_f32 v[52:53], v[52:53], v[68:69], v[56:57]
	v_pk_mul_f32 v[56:57], v[76:77], v[58:59]
	v_pk_mul_f32 v[58:59], v[74:75], v[62:63]
	v_pk_fma_f32 v[54:55], v[54:55], v[70:71], v[60:61]
	v_pk_fma_f32 v[50:51], v[50:51], v[66:67], v[58:59]
	v_pk_fma_f32 v[48:49], v[48:49], v[64:65], v[56:57]
.LBB0_233:
	v_cvt_pk_bf16_f32 v52, v52, v53
	v_cvt_pk_bf16_f32 v53, v54, v55
	s_nop 0
	v_cvt_pk_bf16_f32 v54, v48, v49
	v_lshl_add_u64 v[48:49], v[72:73], 0, s[50:51]
	v_lshlrev_b64 v[48:49], 8, v[48:49]
	v_add_u32_e32 v56, 0x90, v160
	v_lshl_add_u64 v[48:49], v[162:163], 0, v[48:49]
	s_and_b64 vcc, exec, s[2:3]
	v_ashrrev_i32_e32 v57, 31, v56
	v_cvt_pk_bf16_f32 v55, v50, v51
	global_store_dwordx4 v[48:49], v[52:55], off nt
	s_cbranch_vccz .LBB0_263
	v_mov_b32_e32 v48, 1.0
	v_mov_b32_e32 v60, 0
	v_mov_b32_e32 v61, v60
	v_mov_b32_e32 v58, v60
	v_mov_b32_e32 v59, v60
	v_mov_b32_e32 v64, v60
	v_mov_b32_e32 v65, v60
	v_mov_b32_e32 v62, v60
	v_mov_b32_e32 v63, v60
	v_mov_b32_e32 v49, v48
	v_mov_b32_e32 v50, v48
	v_mov_b32_e32 v51, v48
	v_mov_b32_e32 v52, v48
	v_mov_b32_e32 v53, v48
	v_mov_b32_e32 v54, v48
	v_mov_b32_e32 v55, v48
	s_and_b64 vcc, exec, s[2:3]
	s_cbranch_vccnz .LBB0_236

; __device__ __forceinline__ unsigned cvt_pk_bf16(float lo, float hi) { unsigned r; asm volatile("v_cvt_pk_bf16_f32 %0, %1, %2" : "=v"(r) : "v"(lo), "v"(hi)); return r; }
;     __device__ __forceinline__ void operator()(const f32x4 (&acc)[2][2][4][2], const Unit& u, int wr, int wc, int fr, int fq) const {
;     ...
;                 for (int m = 0; m < 4; ++m) { const int row = row0 + ai * HALF + m * 16;
;                     f32x4 cs0 = (f32x4){1.f, 1.f, 1.f, 1.f}, cs1 = cs0, sn0 = (f32x4){0.f, 0.f, 0.f, 0.f}, sn1 = sn0;
;                     if (wc == 0) { const float* rp = rope + (size_t)row * 32 + 8 * (fq & 1); cs0 = *(const f32x4*)rp; cs1 = *(const f32x4*)(rp + 4); sn0 = *(const f32x4*)(rp + 16) * sgn; sn1 = *(const f32x4*)(rp + 20) * sgn; }
; #pragma unroll
;                     for (int bj = 0; bj < 2; ++bj) { f32x4 v0 = acc[ai][bj][m][0], v1 = acc[ai][bj][m][1];
;                         if (wc == 0) { f32x4 p0, p1;
; #pragma unroll
;                             for (int i = 0; i < 4; ++i) { p0[i] = __shfl_xor(v0[i], 32); p1[i] = __shfl_xor(v1[i], 32); }
;                             v0 = v0 * cs0 + p0 * sn0; v1 = v1 * cs1 + p1 * sn1; }
;                         u32x4 w; w.x = cvt_pk_bf16(v0[0], v0[1]); w.y = cvt_pk_bf16(v0[2], v0[3]); w.z = cvt_pk_bf16(v1[0], v1[1]); w.w = cvt_pk_bf16(v1[2], v1[3]);
;                         *(u32x4*)(base + ((size_t)(hp + bj) * T_ROWS + row) * 128 + wc * 32 + 8 * fq) = w; } }
.LBB0_236:
	v_cvt_pk_bf16_f32 v44, v44, v45
	v_cvt_pk_bf16_f32 v45, v46, v47
	s_nop 0
	v_cvt_pk_bf16_f32 v46, v40, v41
	v_lshl_add_u64 v[40:41], v[56:57], 0, s[6:7]
	v_lshlrev_b64 v[40:41], 8, v[40:41]
	v_lshl_add_u64 v[40:41], v[162:163], 0, v[40:41]
	s_and_b64 vcc, exec, s[2:3]
	v_cvt_pk_bf16_f32 v47, v42, v43
	global_store_dwordx4 v[40:41], v[44:47], off nt
	s_cbranch_vccnz .LBB0_238
	v_and_b32_e32 v41, 64, v178
	v_xor_b32_e32 v40, 32, v178
	v_add_u32_e32 v41, 64, v41
	v_cmp_lt_i32_e32 vcc, v40, v41
	s_nop 1
	v_cndmask_b32_e32 v40, v178, v40, vcc
	v_lshlrev_b32_e32 v47, 2, v40
	ds_bpermute_b32 v40, v47, v36
	ds_bpermute_b32 v41, v47, v37
	ds_bpermute_b32 v42, v47, v32
	ds_bpermute_b32 v44, v47, v38
	ds_bpermute_b32 v45, v47, v39
	ds_bpermute_b32 v43, v47, v33
	ds_bpermute_b32 v46, v47, v34
	ds_bpermute_b32 v47, v47, v35
	s_waitcnt lgkmcnt(0)
	v_pk_mul_f32 v[40:41], v[64:65], v[40:41]
	v_pk_mul_f32 v[44:45], v[62:63], v[44:45]
	v_pk_fma_f32 v[36:37], v[36:37], v[52:53], v[40:41]
	v_pk_mul_f32 v[40:41], v[60:61], v[42:43]
	v_pk_mul_f32 v[42:43], v[58:59], v[46:47]
	v_pk_fma_f32 v[38:39], v[38:39], v[54:55], v[44:45]
	v_pk_fma_f32 v[34:35], v[34:35], v[50:51], v[42:43]
	v_pk_fma_f32 v[32:33], v[32:33], v[48:49], v[40:41]
.LBB0_238:
	v_cvt_pk_bf16_f32 v36, v36, v37
	v_cvt_pk_bf16_f32 v37, v38, v39
	s_nop 0
	v_cvt_pk_bf16_f32 v38, v32, v33
	v_lshl_add_u64 v[32:33], v[56:57], 0, s[50:51]
	v_lshlrev_b64 v[32:33], 8, v[32:33]
	v_add_u32_e32 v40, 0xa0, v160
	v_lshl_add_u64 v[32:33], v[162:163], 0, v[32:33]
	s_and_b64 vcc, exec, s[2:3]
	v_ashrrev_i32_e32 v41, 31, v40
	v_cvt_pk_bf16_f32 v39, v34, v35
	global_store_dwordx4 v[32:33], v[36:39], off nt
	s_cbranch_vccz .LBB0_264
	v_mov_b32_e32 v32, 1.0
	v_mov_b32_e32 v44, 0
	v_mov_b32_e32 v45, v44
	v_mov_b32_e32 v42, v44
	v_mov_b32_e32 v43, v44
	v_mov_b32_e32 v48, v44
	v_mov_b32_e32 v49, v44
	v_mov_b32_e32 v46, v44
	v_mov_b32_e32 v47, v44
	v_mov_b32_e32 v33, v32
	v_mov_b32_e32 v34, v32
	v_mov_b32_e32 v35, v32
	v_mov_b32_e32 v36, v32
	v_mov_b32_e32 v37, v32
	v_mov_b32_e32 v38, v32
	v_mov_b32_e32 v39, v32
	s_and_b64 vcc, exec, s[2:3]
	s_cbranch_vccnz .LBB0_241

; __device__ __forceinline__ unsigned cvt_pk_bf16(float lo, float hi) { unsigned r; asm volatile("v_cvt_pk_bf16_f32 %0, %1, %2" : "=v"(r) : "v"(lo), "v"(hi)); return r; }
;     __device__ __forceinline__ void operator()(const f32x4 (&acc)[2][2][4][2], const Unit& u, int wr, int wc, int fr, int fq) const {
;     ...
;                 for (int m = 0; m < 4; ++m) { const int row = row0 + ai * HALF + m * 16;
;                     f32x4 cs0 = (f32x4){1.f, 1.f, 1.f, 1.f}, cs1 = cs0, sn0 = (f32x4){0.f, 0.f, 0.f, 0.f}, sn1 = sn0;
;                     if (wc == 0) { const float* rp = rope + (size_t)row * 32 + 8 * (fq & 1); cs0 = *(const f32x4*)rp; cs1 = *(const f32x4*)(rp + 4); sn0 = *(const f32x4*)(rp + 16) * sgn; sn1 = *(const f32x4*)(rp + 20) * sgn; }
; #pragma unroll
;                     for (int bj = 0; bj < 2; ++bj) { f32x4 v0 = acc[ai][bj][m][0], v1 = acc[ai][bj][m][1];
;                         if (wc == 0) { f32x4 p0, p1;
; #pragma unroll
;                             for (int i = 0; i < 4; ++i) { p0[i] = __shfl_xor(v0[i], 32); p1[i] = __shfl_xor(v1[i], 32); }
;                             v0 = v0 * cs0 + p0 * sn0; v1 = v1 * cs1 + p1 * sn1; }
;                         u32x4 w; w.x = cvt_pk_bf16(v0[0], v0[1]); w.y = cvt_pk_bf16(v0[2], v0[3]); w.z = cvt_pk_bf16(v1[0], v1[1]); w.w = cvt_pk_bf16(v1[2], v1[3]);
;                         *(u32x4*)(base + ((size_t)(hp + bj) * T_ROWS + row) * 128 + wc * 32 + 8 * fq) = w; } }
.LBB0_241:
	v_cvt_pk_bf16_f32 v28, v28, v29
	v_cvt_pk_bf16_f32 v29, v30, v31
	s_nop 0
	v_cvt_pk_bf16_f32 v30, v24, v25
	v_lshl_add_u64 v[24:25], v[40:41], 0, s[6:7]
	v_lshlrev_b64 v[24:25], 8, v[24:25]
	v_lshl_add_u64 v[24:25], v[162:163], 0, v[24:25]
	s_and_b64 vcc, exec, s[2:3]
	v_cvt_pk_bf16_f32 v31, v26, v27
	global_store_dwordx4 v[24:25], v[28:31], off nt
	s_cbranch_vccnz .LBB0_243
	v_and_b32_e32 v25, 64, v178
	v_xor_b32_e32 v24, 32, v178
	v_add_u32_e32 v25, 64, v25
	v_cmp_lt_i32_e32 vcc, v24, v25
	s_nop 1
	v_cndmask_b32_e32 v24, v178, v24, vcc
	v_lshlrev_b32_e32 v31, 2, v24
	ds_bpermute_b32 v24, v31, v20
	ds_bpermute_b32 v25, v31, v21
	ds_bpermute_b32 v26, v31, v16
	ds_bpermute_b32 v28, v31, v22
	ds_bpermute_b32 v29, v31, v23
	ds_bpermute_b32 v27, v31, v17
	ds_bpermute_b32 v30, v31, v18
	ds_bpermute_b32 v31, v31, v19
	s_waitcnt lgkmcnt(0)
	v_pk_mul_f32 v[24:25], v[48:49], v[24:25]
	v_pk_mul_f32 v[28:29], v[46:47], v[28:29]
	v_pk_fma_f32 v[20:21], v[20:21], v[36:37], v[24:25]
	v_pk_mul_f32 v[24:25], v[44:45], v[26:27]
	v_pk_mul_f32 v[26:27], v[42:43], v[30:31]
	v_pk_fma_f32 v[22:23], v[22:23], v[38:39], v[28:29]
	v_pk_fma_f32 v[18:19], v[18:19], v[34:35], v[26:27]
	v_pk_fma_f32 v[16:17], v[16:17], v[32:33], v[24:25]
.LBB0_243:
	v_cvt_pk_bf16_f32 v20, v20, v21
	v_cvt_pk_bf16_f32 v21, v22, v23
	s_nop 0
	v_cvt_pk_bf16_f32 v22, v16, v17
	v_lshl_add_u64 v[16:17], v[40:41], 0, s[50:51]
	v_lshlrev_b64 v[16:17], 8, v[16:17]
	v_add_u32_e32 v24, 0xb0, v160
	v_lshl_add_u64 v[16:17], v[162:163], 0, v[16:17]
	s_and_b64 vcc, exec, s[2:3]
	v_ashrrev_i32_e32 v25, 31, v24
	v_cvt_pk_bf16_f32 v23, v18, v19
	global_store_dwordx4 v[16:17], v[20:23], off nt
	s_cbranch_vccz .LBB0_265
	v_mov_b32_e32 v16, 1.0
	v_mov_b32_e32 v28, 0
	v_mov_b32_e32 v29, v28
	v_mov_b32_e32 v26, v28
	v_mov_b32_e32 v27, v28
	v_mov_b32_e32 v32, v28
	v_mov_b32_e32 v33, v28
	v_mov_b32_e32 v30, v28
	v_mov_b32_e32 v31, v28
	v_mov_b32_e32 v17, v16
	v_mov_b32_e32 v18, v16
	v_mov_b32_e32 v19, v16
	v_mov_b32_e32 v20, v16
	v_mov_b32_e32 v21, v16
	v_mov_b32_e32 v22, v16
	v_mov_b32_e32 v23, v16
	s_and_b64 vcc, exec, s[2:3]
	s_cbranch_vccnz .LBB0_246

; __device__ __forceinline__ unsigned cvt_pk_bf16(float lo, float hi) { unsigned r; asm volatile("v_cvt_pk_bf16_f32 %0, %1, %2" : "=v"(r) : "v"(lo), "v"(hi)); return r; }
; #define PG8_BAR __builtin_amdgcn_s_barrier()
;     __device__ __forceinline__ void operator()(const f32x4 (&acc)[2][2][4][2], const Unit& u, int wr, int wc, int fr, int fq) const {
;     ...
;                 for (int m = 0; m < 4; ++m) { const int row = row0 + ai * HALF + m * 16;
;                     f32x4 cs0 = (f32x4){1.f, 1.f, 1.f, 1.f}, cs1 = cs0, sn0 = (f32x4){0.f, 0.f, 0.f, 0.f}, sn1 = sn0;
;                     if (wc == 0) { const float* rp = rope + (size_t)row * 32 + 8 * (fq & 1); cs0 = *(const f32x4*)rp; cs1 = *(const f32x4*)(rp + 4); sn0 = *(const f32x4*)(rp + 16) * sgn; sn1 = *(const f32x4*)(rp + 20) * sgn; }
; #pragma unroll
;                     for (int bj = 0; bj < 2; ++bj) { f32x4 v0 = acc[ai][bj][m][0], v1 = acc[ai][bj][m][1];
;                         if (wc == 0) { f32x4 p0, p1;
; #pragma unroll
;                             for (int i = 0; i < 4; ++i) { p0[i] = __shfl_xor(v0[i], 32); p1[i] = __shfl_xor(v1[i], 32); }
;                             v0 = v0 * cs0 + p0 * sn0; v1 = v1 * cs1 + p1 * sn1; }
;                         u32x4 w; w.x = cvt_pk_bf16(v0[0], v0[1]); w.y = cvt_pk_bf16(v0[2], v0[3]); w.z = cvt_pk_bf16(v1[0], v1[1]); w.w = cvt_pk_bf16(v1[2], v1[3]);
;                         *(u32x4*)(base + ((size_t)(hp + bj) * T_ROWS + row) * 128 + wc * 32 + 8 * fq) = w; } }
; template <class Epi, class Sched, bool ALIGN_EPI = false, bool SP2 = false>
; __device__ __forceinline__ void gemm_phase(PG8_LAS unsigned char* lds, const Gemm g, const Sched& S, const Epi& E, const int tid_in) {
;     ...
;         if constexpr (ALIGN_EPI) { if (wr == 0) PG8_BAR; }
;         if constexpr (!Epi::AFTER_DRAIN) { E(acc, cur, wr, wc, fr, fq); S.done(cur); }
;         if (!has_next) break;
.LBB0_246:
	v_cvt_pk_bf16_f32 v12, v12, v13
	v_cvt_pk_bf16_f32 v13, v14, v15
	s_nop 0
	v_cvt_pk_bf16_f32 v14, v8, v9
	v_lshl_add_u64 v[8:9], v[24:25], 0, s[6:7]
	v_lshlrev_b64 v[8:9], 8, v[8:9]
	v_lshl_add_u64 v[8:9], v[162:163], 0, v[8:9]
	s_and_b64 vcc, exec, s[2:3]
	v_cvt_pk_bf16_f32 v15, v10, v11
	global_store_dwordx4 v[8:9], v[12:15], off nt
	s_cbranch_vccnz .LBB0_248
	v_and_b32_e32 v9, 64, v178
	v_xor_b32_e32 v8, 32, v178
	v_add_u32_e32 v9, 64, v9
	v_cmp_lt_i32_e32 vcc, v8, v9
	s_nop 1
	v_cndmask_b32_e32 v8, v178, v8, vcc
	v_lshlrev_b32_e32 v15, 2, v8
	ds_bpermute_b32 v8, v15, v4
	ds_bpermute_b32 v9, v15, v5
	ds_bpermute_b32 v10, v15, v0
	ds_bpermute_b32 v12, v15, v6
	ds_bpermute_b32 v13, v15, v7
	ds_bpermute_b32 v11, v15, v1
	ds_bpermute_b32 v14, v15, v2
	ds_bpermute_b32 v15, v15, v3
	s_waitcnt lgkmcnt(0)
	v_pk_mul_f32 v[8:9], v[32:33], v[8:9]
	v_pk_mul_f32 v[12:13], v[30:31], v[12:13]
	v_pk_fma_f32 v[4:5], v[4:5], v[20:21], v[8:9]
	v_pk_mul_f32 v[8:9], v[28:29], v[10:11]
	v_pk_mul_f32 v[10:11], v[26:27], v[14:15]
	v_pk_fma_f32 v[6:7], v[6:7], v[22:23], v[12:13]
	v_pk_fma_f32 v[2:3], v[2:3], v[18:19], v[10:11]
	v_pk_fma_f32 v[0:1], v[0:1], v[16:17], v[8:9]
.LBB0_248:
	v_cvt_pk_bf16_f32 v4, v4, v5
	v_cvt_pk_bf16_f32 v5, v6, v7
	s_nop 0
	v_cvt_pk_bf16_f32 v6, v0, v1
	v_lshl_add_u64 v[0:1], v[24:25], 0, s[50:51]
	v_lshlrev_b64 v[0:1], 8, v[0:1]
	v_lshl_add_u64 v[0:1], v[162:163], 0, v[0:1]
	v_cvt_pk_bf16_f32 v7, v2, v3
	global_store_dwordx4 v[0:1], v[4:7], off nt
	s_andn2_b64 vcc, exec, s[44:45]
	s_mov_b64 s[2:3], -1
	s_cbranch_vccnz .LBB0_195
	s_branch .LBB0_256

; __device__ __forceinline__ unsigned cvt_pk_bf16(float lo, float hi) { unsigned r; asm volatile("v_cvt_pk_bf16_f32 %0, %1, %2" : "=v"(r) : "v"(lo), "v"(hi)); return r; }
;     __device__ __forceinline__ void operator()(const f32x4 (&acc)[2][2][4][2], const Unit& u, int wr, int wc, int fr, int fq) const {
;     ...
;         } else {
;             const int col0 = (pn - 24) * BM + wc * 32 + 8 * fq;
; #pragma unroll
;             for (int ai = 0; ai < 2; ++ai)
; #pragma unroll
;                 for (int m = 0; m < 4; ++m) { const int row = row0 + ai * HALF + m * 16;
; #pragma unroll
;                     for (int bj = 0; bj < 2; ++bj) { const f32x4 v0 = acc[ai][bj][m][0], v1 = acc[ai][bj][m][1];
;                         u32x4 w; w.x = cvt_pk_bf16(v0[0], v0[1]); w.y = cvt_pk_bf16(v0[2], v0[3]); w.z = cvt_pk_bf16(v1[0], v1[1]); w.w = cvt_pk_bf16(v1[2], v1[3]);
;                         *(u32x4*)(R + (size_t)row * R_LD + col0 + bj * HALF) = w; } }
.LBB0_250:
	s_cmp_gt_u32 s50, 23
	s_cbranch_scc0 .LBB0_252
	v_lshl_add_u32 v130, s50, 8, v174
	v_mov_b32_e32 v131, v145
	v_mov_b64_e32 v[128:129], s[10:11]
	v_mad_i64_i32 v[162:163], s[2:3], v160, s72, v[128:129]
	v_lshlrev_b64 v[130:131], 1, v[130:131]
	v_cvt_pk_bf16_f32 v132, v124, v125
	v_cvt_pk_bf16_f32 v133, v126, v127
	v_cvt_pk_bf16_f32 v134, v120, v121
	v_cvt_pk_bf16_f32 v135, v122, v123
	v_lshl_add_u64 v[162:163], v[162:163], 0, v[130:131]
	v_or_b32_e32 v161, 16, v160
	global_store_dwordx4 v[162:163], v[132:135], off nt
	s_nop 1
	v_cvt_pk_bf16_f32 v132, v116, v117
	v_cvt_pk_bf16_f32 v133, v118, v119
	v_cvt_pk_bf16_f32 v134, v112, v113
	v_cvt_pk_bf16_f32 v135, v114, v115
	global_store_dwordx4 v[162:163], v[132:135], off offset:256 nt
	v_mad_i64_i32 v[162:163], s[2:3], v161, s72, v[128:129]
	s_nop 0
	v_cvt_pk_bf16_f32 v132, v108, v109
	v_cvt_pk_bf16_f32 v133, v110, v111
	v_cvt_pk_bf16_f32 v134, v104, v105
	v_cvt_pk_bf16_f32 v135, v106, v107
	v_lshl_add_u64 v[162:163], v[162:163], 0, v[130:131]
	v_or_b32_e32 v161, 32, v160
	global_store_dwordx4 v[162:163], v[132:135], off nt
	s_nop 1
	v_cvt_pk_bf16_f32 v132, v100, v101
	v_cvt_pk_bf16_f32 v133, v102, v103
	v_cvt_pk_bf16_f32 v134, v96, v97
	v_cvt_pk_bf16_f32 v135, v98, v99
	global_store_dwordx4 v[162:163], v[132:135], off offset:256 nt
	v_mad_i64_i32 v[162:163], s[2:3], v161, s72, v[128:129]
	s_nop 0
	v_cvt_pk_bf16_f32 v132, v92, v93
	v_cvt_pk_bf16_f32 v133, v94, v95
	v_cvt_pk_bf16_f32 v134, v88, v89
	v_cvt_pk_bf16_f32 v135, v90, v91
	v_lshl_add_u64 v[162:163], v[162:163], 0, v[130:131]
	v_or_b32_e32 v161, 48, v160
	global_store_dwordx4 v[162:163], v[132:135], off nt
	s_nop 1
	v_cvt_pk_bf16_f32 v132, v84, v85
	v_cvt_pk_bf16_f32 v133, v86, v87
	v_cvt_pk_bf16_f32 v134, v80, v81
	v_cvt_pk_bf16_f32 v135, v82, v83
	global_store_dwordx4 v[162:163], v[132:135], off offset:256 nt
	v_mad_i64_i32 v[162:163], s[2:3], v161, s72, v[128:129]
	s_nop 0
	v_cvt_pk_bf16_f32 v132, v76, v77
	v_cvt_pk_bf16_f32 v133, v78, v79
	v_cvt_pk_bf16_f32 v134, v72, v73
	v_cvt_pk_bf16_f32 v135, v74, v75
	v_lshl_add_u64 v[162:163], v[162:163], 0, v[130:131]
	v_add_u32_e32 v161, 0x80, v160
	global_store_dwordx4 v[162:163], v[132:135], off nt
	s_nop 1
	v_cvt_pk_bf16_f32 v132, v68, v69
	v_cvt_pk_bf16_f32 v133, v70, v71
	v_cvt_pk_bf16_f32 v134, v64, v65
	v_cvt_pk_bf16_f32 v135, v66, v67
	global_store_dwordx4 v[162:163], v[132:135], off offset:256 nt
	v_mad_i64_i32 v[162:163], s[2:3], v161, s72, v[128:129]
	s_nop 0
	v_cvt_pk_bf16_f32 v132, v60, v61
	v_cvt_pk_bf16_f32 v133, v62, v63
	v_cvt_pk_bf16_f32 v134, v56, v57
	v_cvt_pk_bf16_f32 v135, v58, v59
	v_lshl_add_u64 v[162:163], v[162:163], 0, v[130:131]
	v_add_u32_e32 v161, 0x90, v160
	global_store_dwordx4 v[162:163], v[132:135], off nt
	s_nop 1
	v_cvt_pk_bf16_f32 v132, v52, v53
	v_cvt_pk_bf16_f32 v133, v54, v55
	v_cvt_pk_bf16_f32 v134, v48, v49
	v_cvt_pk_bf16_f32 v135, v50, v51
	global_store_dwordx4 v[162:163], v[132:135], off offset:256 nt
	v_mad_i64_i32 v[162:163], s[2:3], v161, s72, v[128:129]
	s_nop 0
	v_cvt_pk_bf16_f32 v132, v44, v45
	v_cvt_pk_bf16_f32 v133, v46, v47
	v_cvt_pk_bf16_f32 v134, v40, v41
	v_cvt_pk_bf16_f32 v135, v42, v43
	v_lshl_add_u64 v[162:163], v[162:163], 0, v[130:131]
	v_add_u32_e32 v161, 0xa0, v160
	global_store_dwordx4 v[162:163], v[132:135], off nt
	s_nop 1
	v_cvt_pk_bf16_f32 v132, v36, v37
	v_cvt_pk_bf16_f32 v133, v38, v39
	v_cvt_pk_bf16_f32 v134, v32, v33
	v_cvt_pk_bf16_f32 v135, v34, v35
	global_store_dwordx4 v[162:163], v[132:135], off offset:256 nt
	v_mad_i64_i32 v[162:163], s[2:3], v161, s72, v[128:129]
	v_add_u32_e32 v161, 0xb0, v160
	v_cvt_pk_bf16_f32 v132, v28, v29
	v_cvt_pk_bf16_f32 v133, v30, v31
	v_cvt_pk_bf16_f32 v134, v24, v25
	v_cvt_pk_bf16_f32 v135, v26, v27
	v_lshl_add_u64 v[162:163], v[162:163], 0, v[130:131]
	v_mad_i64_i32 v[128:129], s[2:3], v161, s72, v[128:129]
	global_store_dwordx4 v[162:163], v[132:135], off nt
	s_mov_b64 s[2:3], 0
	s_nop 0
	v_cvt_pk_bf16_f32 v132, v20, v21
	v_cvt_pk_bf16_f32 v133, v22, v23
	v_cvt_pk_bf16_f32 v134, v16, v17
	v_cvt_pk_bf16_f32 v135, v18, v19
	global_store_dwordx4 v[162:163], v[132:135], off offset:256 nt
	v_lshl_add_u64 v[162:163], v[128:129], 0, v[130:131]
	s_nop 0
	v_cvt_pk_bf16_f32 v132, v12, v13
	v_cvt_pk_bf16_f32 v133, v14, v15
	v_cvt_pk_bf16_f32 v134, v8, v9
	v_cvt_pk_bf16_f32 v135, v10, v11
	global_store_dwordx4 v[162:163], v[132:135], off nt
	v_cvt_pk_bf16_f32 v128, v4, v5
	v_cvt_pk_bf16_f32 v129, v6, v7
	v_cvt_pk_bf16_f32 v130, v0, v1
	v_cvt_pk_bf16_f32 v131, v2, v3
	global_store_dwordx4 v[162:163], v[128:131], off offset:256 nt
; __device__ __forceinline__ unsigned cvt_pk_bf16(float lo, float hi) { unsigned r; asm volatile("v_cvt_pk_bf16_f32 %0, %1, %2" : "=v"(r) : "v"(lo), "v"(hi)); return r; }
;     __device__ __forceinline__ void operator()(const f32x4 (&acc)[2][2][4][2], const Unit& u, int wr, int wc, int fr, int fq) const {
;     ...
;         } else if (pn < 24) {
;             const int hv = (pn - 16) * 2;
; #pragma unroll
;             for (int ai = 0; ai < 2; ++ai)
; #pragma unroll
;                 for (int m = 0; m < 4; ++m) { const int row = row0 + ai * HALF + m * 16;
; #pragma unroll
;                     for (int bj = 0; bj < 2; ++bj) { const f32x4 v0 = acc[ai][bj][m][0], v1 = acc[ai][bj][m][1];
;                         u32x4 w; w.x = cvt_pk_bf16(v0[0], v0[1]); w.y = cvt_pk_bf16(v0[2], v0[3]); w.z = cvt_pk_bf16(v1[0], v1[1]); w.w = cvt_pk_bf16(v1[2], v1[3]);
;                         *(u32x4*)(V + ((size_t)(hv + bj) * T_ROWS + row) * 128 + wc * 32 + 8 * fq) = w; } }
.LBB0_252:
	s_andn2_b64 vcc, exec, s[2:3]
	s_cbranch_vccnz .LBB0_254
	s_lshl_b32 s4, s50, 1
	s_sub_i32 s6, s4, 32
	s_lshl_b64 s[2:3], s[6:7], 21
	v_ashrrev_i32_e32 v161, 31, v160
	s_add_u32 s2, s65, s2
	v_lshlrev_b64 v[128:129], 8, v[160:161]
	s_addc_u32 s3, s67, s3
	s_sub_i32 s6, s4, 31
	v_lshl_add_u64 v[134:135], s[2:3], 0, v[128:129]
	s_mov_b32 s31, s7
	s_lshl_b64 s[4:5], s[6:7], 21
	v_lshl_add_u64 v[134:135], v[134:135], 0, s[30:31]
	s_add_u32 s52, s65, s4
	v_lshl_add_u64 v[134:135], v[134:135], 0, v[144:145]
	s_addc_u32 s53, s67, s5
	v_cvt_pk_bf16_f32 v130, v124, v125
	v_cvt_pk_bf16_f32 v131, v126, v127
	v_cvt_pk_bf16_f32 v132, v120, v121
	v_cvt_pk_bf16_f32 v133, v122, v123
	global_store_dwordx4 v[134:135], v[130:133], off nt
	v_lshl_add_u64 v[134:135], s[52:53], 0, v[128:129]
	v_lshl_add_u64 v[134:135], v[134:135], 0, s[30:31]
	v_cvt_pk_bf16_f32 v130, v116, v117
	v_lshl_add_u64 v[134:135], v[134:135], 0, v[144:145]
	v_cvt_pk_bf16_f32 v131, v118, v119
	v_cvt_pk_bf16_f32 v132, v112, v113
	v_cvt_pk_bf16_f32 v133, v114, v115
	global_store_dwordx4 v[134:135], v[130:133], off nt
	s_nop 1
	v_or_b32_e32 v130, 16, v160
	v_ashrrev_i32_e32 v131, 31, v130
	v_lshlrev_b64 v[134:135], 8, v[130:131]
	v_lshl_add_u64 v[162:163], s[2:3], 0, v[134:135]
	v_lshl_add_u64 v[162:163], v[162:163], 0, s[30:31]
	v_lshl_add_u64 v[134:135], s[52:53], 0, v[134:135]
	v_cvt_pk_bf16_f32 v130, v108, v109
	v_lshl_add_u64 v[162:163], v[162:163], 0, v[144:145]
	v_lshl_add_u64 v[134:135], v[134:135], 0, s[30:31]
	v_cvt_pk_bf16_f32 v131, v110, v111
	v_cvt_pk_bf16_f32 v132, v104, v105
	v_cvt_pk_bf16_f32 v133, v106, v107
	global_store_dwordx4 v[162:163], v[130:133], off nt
	v_lshl_add_u64 v[134:135], v[134:135], 0, v[144:145]
	s_nop 0
	v_cvt_pk_bf16_f32 v130, v100, v101
	v_cvt_pk_bf16_f32 v131, v102, v103
	v_cvt_pk_bf16_f32 v132, v96, v97
	v_cvt_pk_bf16_f32 v133, v98, v99
	global_store_dwordx4 v[134:135], v[130:133], off nt
	s_nop 1
	v_or_b32_e32 v130, 32, v160
	v_ashrrev_i32_e32 v131, 31, v130
	v_lshlrev_b64 v[134:135], 8, v[130:131]
	v_lshl_add_u64 v[162:163], s[2:3], 0, v[134:135]
	v_lshl_add_u64 v[162:163], v[162:163], 0, s[30:31]
	v_lshl_add_u64 v[134:135], s[52:53], 0, v[134:135]
	v_cvt_pk_bf16_f32 v130, v92, v93
	v_lshl_add_u64 v[162:163], v[162:163], 0, v[144:145]
	v_lshl_add_u64 v[134:135], v[134:135], 0, s[30:31]
	v_cvt_pk_bf16_f32 v131, v94, v95
	v_cvt_pk_bf16_f32 v132, v88, v89
	v_cvt_pk_bf16_f32 v133, v90, v91
	global_store_dwordx4 v[162:163], v[130:133], off nt
	v_lshl_add_u64 v[134:135], v[134:135], 0, v[144:145]
	s_nop 0
	v_cvt_pk_bf16_f32 v130, v84, v85
	v_cvt_pk_bf16_f32 v131, v86, v87
	v_cvt_pk_bf16_f32 v132, v80, v81
	v_cvt_pk_bf16_f32 v133, v82, v83
	global_store_dwordx4 v[134:135], v[130:133], off nt
	s_nop 1
	v_or_b32_e32 v130, 48, v160
	v_ashrrev_i32_e32 v131, 31, v130
	v_lshlrev_b64 v[134:135], 8, v[130:131]
	v_lshl_add_u64 v[162:163], s[2:3], 0, v[134:135]
	v_lshl_add_u64 v[134:135], s[52:53], 0, v[134:135]
	v_lshl_add_u64 v[162:163], v[162:163], 0, s[30:31]
	v_lshl_add_u64 v[134:135], v[134:135], 0, s[30:31]
	v_cvt_pk_bf16_f32 v130, v76, v77
	v_cvt_pk_bf16_f32 v131, v78, v79
	v_cvt_pk_bf16_f32 v132, v72, v73
	v_cvt_pk_bf16_f32 v133, v74, v75
	v_lshl_add_u64 v[162:163], v[162:163], 0, v[144:145]
	v_lshl_add_u64 v[134:135], v[134:135], 0, v[144:145]
	global_store_dwordx4 v[162:163], v[130:133], off nt
	s_nop 1
	v_cvt_pk_bf16_f32 v130, v68, v69
	v_cvt_pk_bf16_f32 v131, v70, v71
	v_cvt_pk_bf16_f32 v132, v64, v65
	v_cvt_pk_bf16_f32 v133, v66, v67
	global_store_dwordx4 v[134:135], v[130:133], off nt
	v_lshl_add_u64 v[134:135], v[128:129], 0, s[14:15]
	v_lshl_add_u64 v[162:163], s[2:3], 0, v[134:135]
	v_lshl_add_u64 v[134:135], s[52:53], 0, v[134:135]
	v_lshl_add_u64 v[162:163], v[162:163], 0, s[30:31]
	v_lshl_add_u64 v[134:135], v[134:135], 0, s[30:31]
	v_cvt_pk_bf16_f32 v130, v60, v61
	v_cvt_pk_bf16_f32 v131, v62, v63
	v_cvt_pk_bf16_f32 v132, v56, v57
	v_cvt_pk_bf16_f32 v133, v58, v59
	v_lshl_add_u64 v[162:163], v[162:163], 0, v[144:145]
	v_lshl_add_u64 v[134:135], v[134:135], 0, v[144:145]
	global_store_dwordx4 v[162:163], v[130:133], off nt
	s_nop 1
	v_cvt_pk_bf16_f32 v130, v52, v53
	v_cvt_pk_bf16_f32 v131, v54, v55
	v_cvt_pk_bf16_f32 v132, v48, v49
	v_cvt_pk_bf16_f32 v133, v50, v51
	global_store_dwordx4 v[134:135], v[130:133], off nt
	v_lshl_add_u64 v[134:135], v[128:129], 0, s[34:35]
	v_lshl_add_u64 v[162:163], s[2:3], 0, v[134:135]
	v_lshl_add_u64 v[134:135], s[52:53], 0, v[134:135]
	v_lshl_add_u64 v[162:163], v[162:163], 0, s[30:31]
	v_lshl_add_u64 v[134:135], v[134:135], 0, s[30:31]
	v_cvt_pk_bf16_f32 v130, v44, v45
	v_cvt_pk_bf16_f32 v131, v46, v47
	v_cvt_pk_bf16_f32 v132, v40, v41
	v_cvt_pk_bf16_f32 v133, v42, v43
	v_lshl_add_u64 v[162:163], v[162:163], 0, v[144:145]
	v_lshl_add_u64 v[134:135], v[134:135], 0, v[144:145]
	global_store_dwordx4 v[162:163], v[130:133], off nt
	s_nop 1
	v_cvt_pk_bf16_f32 v130, v36, v37
	v_cvt_pk_bf16_f32 v131, v38, v39
	v_cvt_pk_bf16_f32 v132, v32, v33
	v_cvt_pk_bf16_f32 v133, v34, v35
	global_store_dwordx4 v[134:135], v[130:133], off nt
	v_lshl_add_u64 v[134:135], v[128:129], 0, s[36:37]
	v_lshl_add_u64 v[162:163], s[2:3], 0, v[134:135]
	v_lshl_add_u64 v[162:163], v[162:163], 0, s[30:31]
	v_lshl_add_u64 v[134:135], s[52:53], 0, v[134:135]
	v_cvt_pk_bf16_f32 v130, v28, v29
	v_cvt_pk_bf16_f32 v131, v30, v31
	v_cvt_pk_bf16_f32 v132, v24, v25
	v_cvt_pk_bf16_f32 v133, v26, v27
	v_lshl_add_u64 v[162:163], v[162:163], 0, v[144:145]
	v_lshl_add_u64 v[134:135], v[134:135], 0, s[30:31]
	global_store_dwordx4 v[162:163], v[130:133], off nt
	v_lshl_add_u64 v[134:135], v[134:135], 0, v[144:145]
	s_nop 0
	v_cvt_pk_bf16_f32 v130, v20, v21
	v_cvt_pk_bf16_f32 v131, v22, v23
	v_cvt_pk_bf16_f32 v132, v16, v17
	v_cvt_pk_bf16_f32 v133, v18, v19
	global_store_dwordx4 v[134:135], v[130:133], off nt
	s_nop 1
	v_lshl_add_u64 v[132:133], v[128:129], 0, s[38:39]
	v_lshl_add_u64 v[134:135], s[2:3], 0, v[132:133]
	v_lshl_add_u64 v[132:133], s[52:53], 0, v[132:133]
	v_lshl_add_u64 v[134:135], v[134:135], 0, s[30:31]
	v_lshl_add_u64 v[132:133], v[132:133], 0, s[30:31]
	v_cvt_pk_bf16_f32 v128, v12, v13
	v_cvt_pk_bf16_f32 v129, v14, v15
	v_cvt_pk_bf16_f32 v130, v8, v9
	v_cvt_pk_bf16_f32 v131, v10, v11
	v_lshl_add_u64 v[134:135], v[134:135], 0, v[144:145]
	v_lshl_add_u64 v[132:133], v[132:133], 0, v[144:145]
	global_store_dwordx4 v[134:135], v[128:131], off nt
	s_nop 1
	v_cvt_pk_bf16_f32 v128, v4, v5
	v_cvt_pk_bf16_f32 v129, v6, v7
	v_cvt_pk_bf16_f32 v130, v0, v1
	v_cvt_pk_bf16_f32 v131, v2, v3
	global_store_dwordx4 v[132:133], v[128:131], off nt

; __device__ __forceinline__ unsigned cvt_pk_bf16(float lo, float hi) { unsigned r; asm volatile("v_cvt_pk_bf16_f32 %0, %1, %2" : "=v"(r) : "v"(lo), "v"(hi)); return r; }
; __device__ __forceinline__ float sigm(float x) { return __builtin_amdgcn_rcpf(1.0f + __expf(-x)); }
; __device__ __forceinline__ float swiglu1(float g, float l) { g = fminf(g, 7.0f); l = fminf(fmaxf(l, -7.0f), 7.0f); return g * sigm(1.702f * g) * (l + 1.0f); }
;     __device__ __forceinline__ void operator()(const f32x4 (&acc)[2][2][4][2], const Unit& u, int wr, int wc, int fr, int fq) const {
;         const int row0 = u.pm * BM + wr * 64 + fr, col0 = u.pn * BM + wc * 32 + 8 * fq; const float* bb = bias + (size_t)u.e * 4096;
;         f32x4 bv[2][2];
; #pragma unroll
;         for (int bj = 0; bj < 2; ++bj)
; #pragma unroll
;             for (int n = 0; n < 2; ++n) bv[bj][n] = *(const f32x4*)(bb + col0 + bj * HALF + 4 * n);
; #pragma unroll
;         for (int ai = 0; ai < 2; ++ai)
; #pragma unroll
;             for (int m = 0; m < 4; ++m) { const int row = row0 + ai * HALF + m * 16;
; #pragma unroll
;                 for (int bj = 0; bj < 2; ++bj) { const f32x4 v0 = acc[ai][bj][m][0] + bv[bj][0], v1 = acc[ai][bj][m][1] + bv[bj][1];
;                     u32x2 w; w.x = cvt_pk_bf16(swiglu1(v0[0], v0[1]), swiglu1(v0[2], v0[3])); w.y = cvt_pk_bf16(swiglu1(v1[0], v1[1]), swiglu1(v1[2], v1[3]));
;                     *(u32x2*)(O + (size_t)row * 2048 + ((col0 + bj * HALF) >> 1)) = w; } }
.LBB0_2206:
	v_ashrrev_i32_e32 v89, 31, v88
	v_lshl_or_b32 v154, s56, 8, v166
	v_lshlrev_b64 v[88:89], 14, v[88:89]
	v_lshl_add_u64 v[88:89], s[12:13], 0, v[88:89]
	v_ashrrev_i32_e32 v155, 31, v154
	v_lshl_add_u64 v[88:89], v[154:155], 2, v[88:89]
	global_load_dwordx4 v[108:111], v[88:89], off
	global_load_dwordx4 v[104:107], v[88:89], off offset:16
	global_load_dwordx4 v[92:95], v[88:89], off offset:512
	s_nop 0
	global_load_dwordx4 v[88:91], v[88:89], off offset:528
	v_lshl_add_u32 v158, s5, 8, v164
	v_ashrrev_i32_e32 v159, 31, v158
	v_ashrrev_i32_e32 v154, 1, v154
	v_lshlrev_b64 v[156:157], 12, v[158:159]
	v_ashrrev_i32_e32 v155, 31, v154
	v_lshl_add_u64 v[176:177], s[26:27], 0, v[156:157]
	v_lshlrev_b64 v[156:157], 1, v[154:155]
	v_lshl_add_u64 v[154:155], v[176:177], 0, v[156:157]
	s_waitcnt vmcnt(0)
	v_pk_add_f32 v[140:141], v[140:141], v[108:109]
	v_pk_add_f32 v[142:143], v[142:143], v[110:111]
	v_pk_add_f32 v[132:133], v[132:133], v[92:93]
	v_pk_add_f32 v[128:129], v[128:129], v[88:89]
	v_min_f32_e32 v140, 0x40e00000, v140
	v_pk_add_f32 v[138:139], v[138:139], v[106:107]
	v_pk_add_f32 v[136:137], v[136:137], v[104:105]
	v_pk_add_f32 v[134:135], v[134:135], v[94:95]
	v_med3_f32 v141, v141, s75, v170
	v_min_f32_e32 v142, 0x40e00000, v142
	v_min_f32_e32 v132, 0x40e00000, v132
	v_min_f32_e32 v148, 0x40e00000, v128
	v_mul_f32_e32 v128, 0x3fd9db23, v140
	v_min_f32_e32 v136, 0x40e00000, v136
	v_min_f32_e32 v138, 0x40e00000, v138
	v_min_f32_e32 v134, 0x40e00000, v134
	v_med3_f32 v151, v129, s75, v170
	v_add_f32_e32 v129, 1.0, v141
	v_mul_f32_e32 v141, 0x3fd9db23, v142
	v_mul_f32_e32 v176, 0x3fd9db23, v132
	v_mul_f32_e32 v128, 0xbfb8aa3b, v128
	v_mul_f32_e32 v159, 0x3fd9db23, v136
	v_mul_f32_e32 v175, 0x3fd9db23, v138
	v_mul_f32_e32 v177, 0x3fd9db23, v134
	v_mul_f32_e32 v141, 0xbfb8aa3b, v141
	v_mul_f32_e32 v176, 0xbfb8aa3b, v176
	v_exp_f32_e32 v128, v128
	v_mul_f32_e32 v159, 0xbfb8aa3b, v159
	v_mul_f32_e32 v175, 0xbfb8aa3b, v175
	v_mul_f32_e32 v177, 0xbfb8aa3b, v177
	v_exp_f32_e32 v141, v141
	v_exp_f32_e32 v176, v176
	v_exp_f32_e32 v159, v159
	v_exp_f32_e32 v175, v175
	v_exp_f32_e32 v177, v177
	v_pk_add_f32 v[130:131], v[130:131], v[90:91]
	v_add_f32_e32 v128, 1.0, v128
	v_min_f32_e32 v130, 0x40e00000, v130
	v_mul_f32_e32 v178, 0x3fd9db23, v148
	v_add_f32_e32 v141, 1.0, v141
	v_add_f32_e32 v176, 1.0, v176
	v_rcp_f32_e32 v128, v128
	v_mul_f32_e32 v179, 0x3fd9db23, v130
	v_mul_f32_e32 v178, 0xbfb8aa3b, v178
	v_add_f32_e32 v159, 1.0, v159
	v_add_f32_e32 v175, 1.0, v175
	v_add_f32_e32 v177, 1.0, v177
	v_rcp_f32_e32 v141, v141
	v_rcp_f32_e32 v176, v176
	v_mul_f32_e32 v179, 0xbfb8aa3b, v179
	v_exp_f32_e32 v178, v178
	v_rcp_f32_e32 v159, v159
	v_rcp_f32_e32 v175, v175
	v_rcp_f32_e32 v177, v177
	v_exp_f32_e32 v179, v179
	v_med3_f32 v143, v143, s75, v170
	v_med3_f32 v133, v133, s75, v170
	v_mul_f32_e32 v128, v140, v128
	v_med3_f32 v137, v137, s75, v170
	v_med3_f32 v139, v139, s75, v170
	v_med3_f32 v135, v135, s75, v170
	v_add_f32_e32 v143, 1.0, v143
	v_add_f32_e32 v133, 1.0, v133
	v_mul_f32_e32 v140, v142, v141
	v_mul_f32_e32 v132, v132, v176
	v_mul_f32_e32 v128, v129, v128
	v_add_f32_e32 v137, 1.0, v137
	v_add_f32_e32 v139, 1.0, v139
	v_add_f32_e32 v135, 1.0, v135
	v_add_f32_e32 v178, 1.0, v178
	v_mul_f32_e32 v136, v136, v159
	v_mul_f32_e32 v138, v138, v175
	v_mul_f32_e32 v134, v134, v177
	v_mul_f32_e32 v129, v143, v140
	v_mul_f32_e32 v132, v133, v132
	v_cvt_pk_bf16_f32 v128, v128, v129
	v_rcp_f32_e32 v178, v178
	v_mul_f32_e32 v136, v137, v136
	v_mul_f32_e32 v137, v139, v138
	v_mul_f32_e32 v133, v135, v134
	v_cvt_pk_bf16_f32 v129, v136, v137
	global_store_dwordx2 v[154:155], v[128:129], off nt
	v_cvt_pk_bf16_f32 v128, v132, v133
	v_add_f32_e32 v132, 1.0, v179
	v_rcp_f32_e32 v132, v132
	v_mul_f32_e32 v129, v148, v178
	v_add_f32_e32 v133, 1.0, v151
	v_med3_f32 v131, v131, s75, v170
	v_mul_f32_e32 v129, v133, v129
	v_mul_f32_e32 v130, v130, v132
	v_add_f32_e32 v131, 1.0, v131
	v_pk_add_f32 v[124:125], v[124:125], v[108:109]
	v_mul_f32_e32 v130, v131, v130
	v_cvt_pk_bf16_f32 v129, v129, v130
	v_min_f32_e32 v124, 0x40e00000, v124
	global_store_dwordx2 v[154:155], v[128:129], off offset:128 nt
	v_mul_f32_e32 v129, 0x3fd9db23, v124
	v_mul_f32_e32 v129, 0xbfb8aa3b, v129
	v_exp_f32_e32 v130, v129
	v_pk_add_f32 v[126:127], v[126:127], v[110:111]
	v_med3_f32 v125, v125, s75, v170
	v_min_f32_e32 v126, 0x40e00000, v126
	v_add_f32_e32 v130, 1.0, v130
	v_rcp_f32_e32 v130, v130
	v_pk_add_f32 v[120:121], v[120:121], v[104:105]
	v_add_f32_e32 v125, 1.0, v125
	v_pk_add_f32 v[122:123], v[122:123], v[106:107]
	v_mul_f32_e32 v124, v124, v130
	v_mul_f32_e32 v130, 0x3fd9db23, v126
	v_mul_f32_e32 v130, 0xbfb8aa3b, v130
	v_exp_f32_e32 v130, v130
	v_mul_f32_e32 v124, v125, v124
	v_med3_f32 v125, v127, s75, v170
	v_add_f32_e32 v125, 1.0, v125
	v_add_f32_e32 v127, 1.0, v130
	v_min_f32_e32 v130, 0x40e00000, v120
	v_mul_f32_e32 v120, 0x3fd9db23, v130
	v_mul_f32_e32 v120, 0xbfb8aa3b, v120
	v_rcp_f32_e32 v127, v127
	v_exp_f32_e32 v120, v120
	v_min_f32_e32 v122, 0x40e00000, v122
	v_med3_f32 v121, v121, s75, v170
	v_mul_f32_e32 v126, v126, v127
	v_add_f32_e32 v120, 1.0, v120
	v_mul_f32_e32 v125, v125, v126
	v_rcp_f32_e32 v126, v120
	v_mul_f32_e32 v120, 0x3fd9db23, v122
	v_mul_f32_e32 v120, 0xbfb8aa3b, v120
	v_exp_f32_e32 v127, v120
	v_cvt_pk_bf16_f32 v120, v124, v125
	v_pk_add_f32 v[116:117], v[116:117], v[92:93]
	v_mul_f32_e32 v124, v130, v126
	v_add_f32_e32 v125, 1.0, v127
	v_rcp_f32_e32 v125, v125
	v_add_f32_e32 v121, 1.0, v121
	v_min_f32_e32 v116, 0x40e00000, v116
	v_mul_f32_e32 v121, v121, v124
	v_mul_f32_e32 v124, 0x3fd9db23, v116
	v_or_b32_e32 v128, 16, v158
; __device__ __forceinline__ unsigned cvt_pk_bf16(float lo, float hi) { unsigned r; asm volatile("v_cvt_pk_bf16_f32 %0, %1, %2" : "=v"(r) : "v"(lo), "v"(hi)); return r; }
; __device__ __forceinline__ float sigm(float x) { return __builtin_amdgcn_rcpf(1.0f + __expf(-x)); }
; __device__ __forceinline__ float swiglu1(float g, float l) { g = fminf(g, 7.0f); l = fminf(fmaxf(l, -7.0f), 7.0f); return g * sigm(1.702f * g) * (l + 1.0f); }
;     __device__ __forceinline__ void operator()(const f32x4 (&acc)[2][2][4][2], const Unit& u, int wr, int wc, int fr, int fq) const {
;     ...
;             for (int m = 0; m < 4; ++m) { const int row = row0 + ai * HALF + m * 16;
; #pragma unroll
;                 for (int bj = 0; bj < 2; ++bj) { const f32x4 v0 = acc[ai][bj][m][0] + bv[bj][0], v1 = acc[ai][bj][m][1] + bv[bj][1];
;                     u32x2 w; w.x = cvt_pk_bf16(swiglu1(v0[0], v0[1]), swiglu1(v0[2], v0[3])); w.y = cvt_pk_bf16(swiglu1(v1[0], v1[1]), swiglu1(v1[2], v1[3]));
;                     *(u32x2*)(O + (size_t)row * 2048 + ((col0 + bj * HALF) >> 1)) = w; } }
	v_med3_f32 v123, v123, s75, v170
	v_mul_f32_e32 v124, 0xbfb8aa3b, v124
	v_ashrrev_i32_e32 v129, 31, v128
	v_mul_f32_e32 v122, v122, v125
	v_add_f32_e32 v123, 1.0, v123
	v_exp_f32_e32 v124, v124
	v_lshlrev_b64 v[128:129], 12, v[128:129]
	v_mul_f32_e32 v122, v123, v122
	v_cvt_pk_bf16_f32 v121, v121, v122
	v_lshl_add_u64 v[122:123], s[26:27], 0, v[128:129]
	v_lshl_add_u64 v[122:123], v[122:123], 0, v[156:157]
	global_store_dwordx2 v[122:123], v[120:121], off nt
	v_add_f32_e32 v120, 1.0, v124
	v_rcp_f32_e32 v120, v120
	v_pk_add_f32 v[118:119], v[118:119], v[94:95]
	v_med3_f32 v117, v117, s75, v170
	v_min_f32_e32 v118, 0x40e00000, v118
	v_mul_f32_e32 v116, v116, v120
	v_mul_f32_e32 v120, 0x3fd9db23, v118
	v_mul_f32_e32 v120, 0xbfb8aa3b, v120
	v_exp_f32_e32 v120, v120
	v_pk_add_f32 v[112:113], v[112:113], v[88:89]
	v_add_f32_e32 v117, 1.0, v117
	v_mul_f32_e32 v116, v117, v116
	v_med3_f32 v117, v119, s75, v170
	v_add_f32_e32 v119, 1.0, v120
	v_min_f32_e32 v120, 0x40e00000, v112
	v_mul_f32_e32 v112, 0x3fd9db23, v120
	v_mul_f32_e32 v112, 0xbfb8aa3b, v112
	v_rcp_f32_e32 v119, v119
	v_exp_f32_e32 v112, v112
	v_pk_add_f32 v[114:115], v[114:115], v[90:91]
	v_add_f32_e32 v117, 1.0, v117
	v_mul_f32_e32 v118, v118, v119
	v_add_f32_e32 v112, 1.0, v112
	v_min_f32_e32 v114, 0x40e00000, v114
	v_mul_f32_e32 v117, v117, v118
	v_rcp_f32_e32 v118, v112
	v_mul_f32_e32 v112, 0x3fd9db23, v114
	v_mul_f32_e32 v112, 0xbfb8aa3b, v112
	v_exp_f32_e32 v119, v112
	v_cvt_pk_bf16_f32 v112, v116, v117
	v_med3_f32 v113, v113, s75, v170
	v_mul_f32_e32 v116, v120, v118
	v_add_f32_e32 v117, 1.0, v119
	v_rcp_f32_e32 v117, v117
	v_add_f32_e32 v113, 1.0, v113
	v_med3_f32 v115, v115, s75, v170
	v_mul_f32_e32 v113, v113, v116
	v_mul_f32_e32 v114, v114, v117
	v_add_f32_e32 v115, 1.0, v115
	v_pk_add_f32 v[100:101], v[100:101], v[108:109]
	v_mul_f32_e32 v114, v115, v114
	v_cvt_pk_bf16_f32 v113, v113, v114
	v_min_f32_e32 v100, 0x40e00000, v100
	global_store_dwordx2 v[122:123], v[112:113], off offset:128 nt
	v_mul_f32_e32 v113, 0x3fd9db23, v100
	v_mul_f32_e32 v113, 0xbfb8aa3b, v113
	v_exp_f32_e32 v114, v113
	v_pk_add_f32 v[102:103], v[102:103], v[110:111]
	v_med3_f32 v101, v101, s75, v170
	v_min_f32_e32 v102, 0x40e00000, v102
	v_add_f32_e32 v114, 1.0, v114
	v_rcp_f32_e32 v114, v114
	v_pk_add_f32 v[96:97], v[96:97], v[104:105]
	v_add_f32_e32 v101, 1.0, v101
	v_pk_add_f32 v[98:99], v[98:99], v[106:107]
	v_mul_f32_e32 v100, v100, v114
	v_mul_f32_e32 v114, 0x3fd9db23, v102
	v_mul_f32_e32 v114, 0xbfb8aa3b, v114
	v_exp_f32_e32 v114, v114
	v_mul_f32_e32 v100, v101, v100
	v_med3_f32 v101, v103, s75, v170
	v_add_f32_e32 v101, 1.0, v101
	v_add_f32_e32 v103, 1.0, v114
	v_min_f32_e32 v114, 0x40e00000, v96
	v_mul_f32_e32 v96, 0x3fd9db23, v114
	v_mul_f32_e32 v96, 0xbfb8aa3b, v96
	v_rcp_f32_e32 v103, v103
	v_exp_f32_e32 v96, v96
	v_min_f32_e32 v98, 0x40e00000, v98
	v_med3_f32 v97, v97, s75, v170
	v_mul_f32_e32 v102, v102, v103
	v_add_f32_e32 v96, 1.0, v96
	v_mul_f32_e32 v101, v101, v102
	v_rcp_f32_e32 v102, v96
	v_mul_f32_e32 v96, 0x3fd9db23, v98
	v_mul_f32_e32 v96, 0xbfb8aa3b, v96
	v_exp_f32_e32 v103, v96
	v_cvt_pk_bf16_f32 v96, v100, v101
	v_pk_add_f32 v[84:85], v[84:85], v[92:93]
	v_mul_f32_e32 v100, v114, v102
	v_add_f32_e32 v101, 1.0, v103
	v_rcp_f32_e32 v101, v101
	v_add_f32_e32 v97, 1.0, v97
	v_min_f32_e32 v84, 0x40e00000, v84
	v_mul_f32_e32 v97, v97, v100
	v_mul_f32_e32 v100, 0x3fd9db23, v84
	v_or_b32_e32 v112, 32, v158
	v_med3_f32 v99, v99, s75, v170
	v_mul_f32_e32 v100, 0xbfb8aa3b, v100
	v_ashrrev_i32_e32 v113, 31, v112
	v_mul_f32_e32 v98, v98, v101
	v_add_f32_e32 v99, 1.0, v99
	v_exp_f32_e32 v100, v100
	v_lshlrev_b64 v[112:113], 12, v[112:113]
	v_mul_f32_e32 v98, v99, v98
	v_cvt_pk_bf16_f32 v97, v97, v98
	v_lshl_add_u64 v[98:99], s[26:27], 0, v[112:113]
	v_lshl_add_u64 v[98:99], v[98:99], 0, v[156:157]
	global_store_dwordx2 v[98:99], v[96:97], off nt
	v_add_f32_e32 v96, 1.0, v100
	v_rcp_f32_e32 v96, v96
	v_pk_add_f32 v[86:87], v[86:87], v[94:95]
	v_med3_f32 v85, v85, s75, v170
	v_min_f32_e32 v86, 0x40e00000, v86
	v_mul_f32_e32 v84, v84, v96
	v_mul_f32_e32 v96, 0x3fd9db23, v86
	v_mul_f32_e32 v96, 0xbfb8aa3b, v96
	v_exp_f32_e32 v96, v96
	v_pk_add_f32 v[80:81], v[80:81], v[88:89]
	v_add_f32_e32 v85, 1.0, v85
	v_mul_f32_e32 v84, v85, v84
	v_med3_f32 v85, v87, s75, v170
	v_add_f32_e32 v87, 1.0, v96
	v_min_f32_e32 v96, 0x40e00000, v80
	v_mul_f32_e32 v80, 0x3fd9db23, v96
	v_mul_f32_e32 v80, 0xbfb8aa3b, v80
	v_rcp_f32_e32 v87, v87
	v_exp_f32_e32 v80, v80
	v_pk_add_f32 v[82:83], v[82:83], v[90:91]
	v_add_f32_e32 v85, 1.0, v85
	v_mul_f32_e32 v86, v86, v87
	v_add_f32_e32 v80, 1.0, v80
	v_min_f32_e32 v82, 0x40e00000, v82
	v_mul_f32_e32 v85, v85, v86
	v_rcp_f32_e32 v86, v80
	v_mul_f32_e32 v80, 0x3fd9db23, v82
	v_mul_f32_e32 v80, 0xbfb8aa3b, v80
	v_exp_f32_e32 v87, v80
	v_cvt_pk_bf16_f32 v80, v84, v85
	v_med3_f32 v81, v81, s75, v170
	v_mul_f32_e32 v84, v96, v86
	v_add_f32_e32 v85, 1.0, v87
	v_rcp_f32_e32 v85, v85
	v_add_f32_e32 v81, 1.0, v81
	v_med3_f32 v83, v83, s75, v170
	v_mul_f32_e32 v81, v81, v84
	v_mul_f32_e32 v82, v82, v85
	v_add_f32_e32 v83, 1.0, v83
	v_pk_add_f32 v[76:77], v[76:77], v[108:109]
	v_mul_f32_e32 v82, v83, v82
	v_cvt_pk_bf16_f32 v81, v81, v82
	v_min_f32_e32 v76, 0x40e00000, v76
	global_store_dwordx2 v[98:99], v[80:81], off offset:128 nt
	v_mul_f32_e32 v81, 0x3fd9db23, v76
	v_mul_f32_e32 v81, 0xbfb8aa3b, v81
	v_exp_f32_e32 v82, v81
	v_pk_add_f32 v[78:79], v[78:79], v[110:111]
	v_med3_f32 v77, v77, s75, v170
	v_min_f32_e32 v78, 0x40e00000, v78
	v_add_f32_e32 v82, 1.0, v82
	v_rcp_f32_e32 v82, v82
	v_pk_add_f32 v[72:73], v[72:73], v[104:105]
	v_add_f32_e32 v77, 1.0, v77
; __device__ __forceinline__ unsigned cvt_pk_bf16(float lo, float hi) { unsigned r; asm volatile("v_cvt_pk_bf16_f32 %0, %1, %2" : "=v"(r) : "v"(lo), "v"(hi)); return r; }
; __device__ __forceinline__ float sigm(float x) { return __builtin_amdgcn_rcpf(1.0f + __expf(-x)); }
; __device__ __forceinline__ float swiglu1(float g, float l) { g = fminf(g, 7.0f); l = fminf(fmaxf(l, -7.0f), 7.0f); return g * sigm(1.702f * g) * (l + 1.0f); }
;     __device__ __forceinline__ void operator()(const f32x4 (&acc)[2][2][4][2], const Unit& u, int wr, int wc, int fr, int fq) const {
;     ...
;             for (int m = 0; m < 4; ++m) { const int row = row0 + ai * HALF + m * 16;
; #pragma unroll
;                 for (int bj = 0; bj < 2; ++bj) { const f32x4 v0 = acc[ai][bj][m][0] + bv[bj][0], v1 = acc[ai][bj][m][1] + bv[bj][1];
;                     u32x2 w; w.x = cvt_pk_bf16(swiglu1(v0[0], v0[1]), swiglu1(v0[2], v0[3])); w.y = cvt_pk_bf16(swiglu1(v1[0], v1[1]), swiglu1(v1[2], v1[3]));
;                     *(u32x2*)(O + (size_t)row * 2048 + ((col0 + bj * HALF) >> 1)) = w; } }
	v_pk_add_f32 v[74:75], v[74:75], v[106:107]
	v_mul_f32_e32 v76, v76, v82
	v_mul_f32_e32 v82, 0x3fd9db23, v78
	v_mul_f32_e32 v82, 0xbfb8aa3b, v82
	v_exp_f32_e32 v82, v82
	v_mul_f32_e32 v76, v77, v76
	v_med3_f32 v77, v79, s75, v170
	v_add_f32_e32 v77, 1.0, v77
	v_add_f32_e32 v79, 1.0, v82
	v_min_f32_e32 v82, 0x40e00000, v72
	v_mul_f32_e32 v72, 0x3fd9db23, v82
	v_mul_f32_e32 v72, 0xbfb8aa3b, v72
	v_rcp_f32_e32 v79, v79
	v_exp_f32_e32 v72, v72
	v_min_f32_e32 v74, 0x40e00000, v74
	v_med3_f32 v73, v73, s75, v170
	v_mul_f32_e32 v78, v78, v79
	v_add_f32_e32 v72, 1.0, v72
	v_mul_f32_e32 v77, v77, v78
	v_rcp_f32_e32 v78, v72
	v_mul_f32_e32 v72, 0x3fd9db23, v74
	v_mul_f32_e32 v72, 0xbfb8aa3b, v72
	v_exp_f32_e32 v79, v72
	v_cvt_pk_bf16_f32 v72, v76, v77
	v_pk_add_f32 v[68:69], v[68:69], v[92:93]
	v_mul_f32_e32 v76, v82, v78
	v_add_f32_e32 v77, 1.0, v79
	v_rcp_f32_e32 v77, v77
	v_add_f32_e32 v73, 1.0, v73
	v_min_f32_e32 v68, 0x40e00000, v68
	v_mul_f32_e32 v73, v73, v76
	v_mul_f32_e32 v76, 0x3fd9db23, v68
	v_or_b32_e32 v80, 48, v158
	v_med3_f32 v75, v75, s75, v170
	v_mul_f32_e32 v76, 0xbfb8aa3b, v76
	v_ashrrev_i32_e32 v81, 31, v80
	v_mul_f32_e32 v74, v74, v77
	v_add_f32_e32 v75, 1.0, v75
	v_exp_f32_e32 v76, v76
	v_lshlrev_b64 v[80:81], 12, v[80:81]
	v_mul_f32_e32 v74, v75, v74
	v_cvt_pk_bf16_f32 v73, v73, v74
	v_lshl_add_u64 v[74:75], s[26:27], 0, v[80:81]
	v_lshl_add_u64 v[74:75], v[74:75], 0, v[156:157]
	global_store_dwordx2 v[74:75], v[72:73], off nt
	v_add_f32_e32 v72, 1.0, v76
	v_rcp_f32_e32 v72, v72
	v_pk_add_f32 v[70:71], v[70:71], v[94:95]
	v_med3_f32 v69, v69, s75, v170
	v_min_f32_e32 v70, 0x40e00000, v70
	v_mul_f32_e32 v68, v68, v72
	v_mul_f32_e32 v72, 0x3fd9db23, v70
	v_mul_f32_e32 v72, 0xbfb8aa3b, v72
	v_exp_f32_e32 v72, v72
	v_pk_add_f32 v[64:65], v[64:65], v[88:89]
	v_add_f32_e32 v69, 1.0, v69
	v_mul_f32_e32 v68, v69, v68
	v_med3_f32 v69, v71, s75, v170
	v_add_f32_e32 v71, 1.0, v72
	v_min_f32_e32 v72, 0x40e00000, v64
	v_mul_f32_e32 v64, 0x3fd9db23, v72
	v_mul_f32_e32 v64, 0xbfb8aa3b, v64
	v_rcp_f32_e32 v71, v71
	v_exp_f32_e32 v64, v64
	v_pk_add_f32 v[66:67], v[66:67], v[90:91]
	v_add_f32_e32 v69, 1.0, v69
	v_mul_f32_e32 v70, v70, v71
	v_add_f32_e32 v64, 1.0, v64
	v_min_f32_e32 v66, 0x40e00000, v66
	v_mul_f32_e32 v69, v69, v70
	v_rcp_f32_e32 v70, v64
	v_mul_f32_e32 v64, 0x3fd9db23, v66
	v_mul_f32_e32 v64, 0xbfb8aa3b, v64
	v_exp_f32_e32 v71, v64
	v_cvt_pk_bf16_f32 v64, v68, v69
	v_med3_f32 v67, v67, s75, v170
	v_pk_add_f32 v[60:61], v[60:61], v[108:109]
	v_add_f32_e32 v69, 1.0, v71
	v_rcp_f32_e32 v69, v69
	v_add_f32_e32 v67, 1.0, v67
	v_min_f32_e32 v60, 0x40e00000, v60
	v_med3_f32 v65, v65, s75, v170
	v_mul_f32_e32 v66, v66, v69
	v_mul_f32_e32 v66, v67, v66
	v_mul_f32_e32 v67, 0x3fd9db23, v60
	v_mul_f32_e32 v67, 0xbfb8aa3b, v67
	v_exp_f32_e32 v67, v67
	v_mul_f32_e32 v68, v72, v70
	v_add_f32_e32 v65, 1.0, v65
	v_mul_f32_e32 v65, v65, v68
	v_cvt_pk_bf16_f32 v65, v65, v66
	global_store_dwordx2 v[74:75], v[64:65], off offset:128 nt
	v_add_f32_e32 v64, 1.0, v67
	v_rcp_f32_e32 v64, v64
	v_pk_add_f32 v[62:63], v[62:63], v[110:111]
	v_med3_f32 v61, v61, s75, v170
	v_min_f32_e32 v62, 0x40e00000, v62
	v_mul_f32_e32 v60, v60, v64
	v_mul_f32_e32 v64, 0x3fd9db23, v62
	v_mul_f32_e32 v64, 0xbfb8aa3b, v64
	v_exp_f32_e32 v64, v64
	v_pk_add_f32 v[56:57], v[56:57], v[104:105]
	v_add_f32_e32 v61, 1.0, v61
	v_mul_f32_e32 v60, v61, v60
	v_med3_f32 v61, v63, s75, v170
	v_add_f32_e32 v63, 1.0, v64
	v_min_f32_e32 v64, 0x40e00000, v56
	v_mul_f32_e32 v56, 0x3fd9db23, v64
	v_mul_f32_e32 v56, 0xbfb8aa3b, v56
	v_rcp_f32_e32 v63, v63
	v_exp_f32_e32 v56, v56
	v_pk_add_f32 v[58:59], v[58:59], v[106:107]
	v_add_f32_e32 v61, 1.0, v61
	v_mul_f32_e32 v62, v62, v63
	v_add_f32_e32 v56, 1.0, v56
	v_min_f32_e32 v58, 0x40e00000, v58
	v_mul_f32_e32 v61, v61, v62
	v_rcp_f32_e32 v62, v56
	v_mul_f32_e32 v56, 0x3fd9db23, v58
	v_mul_f32_e32 v56, 0xbfb8aa3b, v56
	v_exp_f32_e32 v63, v56
	v_med3_f32 v57, v57, s75, v170
	v_pk_add_f32 v[52:53], v[52:53], v[92:93]
	v_cvt_pk_bf16_f32 v56, v60, v61
	v_mul_f32_e32 v60, v64, v62
	v_add_f32_e32 v57, 1.0, v57
	v_min_f32_e32 v52, 0x40e00000, v52
	v_add_f32_e32 v61, 1.0, v63
	v_mul_f32_e32 v57, v57, v60
	v_mul_f32_e32 v60, 0x3fd9db23, v52
	v_rcp_f32_e32 v61, v61
	v_mul_f32_e32 v60, 0xbfb8aa3b, v60
	v_exp_f32_e32 v62, v60
	v_med3_f32 v59, v59, s75, v170
	v_add_co_u32_e32 v60, vcc, s76, v154
	v_mul_f32_e32 v58, v58, v61
	v_add_f32_e32 v59, 1.0, v59
	v_addc_co_u32_e32 v61, vcc, 0, v155, vcc
	v_mul_f32_e32 v58, v59, v58
	v_cvt_pk_bf16_f32 v57, v57, v58
	global_store_dwordx2 v[60:61], v[56:57], off nt
	v_add_f32_e32 v56, 1.0, v62
	v_rcp_f32_e32 v56, v56
	v_pk_add_f32 v[54:55], v[54:55], v[94:95]
	v_med3_f32 v53, v53, s75, v170
	v_min_f32_e32 v54, 0x40e00000, v54
	v_mul_f32_e32 v52, v52, v56
	v_mul_f32_e32 v56, 0x3fd9db23, v54
	v_mul_f32_e32 v56, 0xbfb8aa3b, v56
	v_exp_f32_e32 v56, v56
	v_pk_add_f32 v[48:49], v[48:49], v[88:89]
	v_add_f32_e32 v53, 1.0, v53
	v_mul_f32_e32 v52, v53, v52
	v_med3_f32 v53, v55, s75, v170
	v_add_f32_e32 v55, 1.0, v56
	v_min_f32_e32 v56, 0x40e00000, v48
	v_mul_f32_e32 v48, 0x3fd9db23, v56
	v_mul_f32_e32 v48, 0xbfb8aa3b, v48
	v_rcp_f32_e32 v55, v55
	v_exp_f32_e32 v48, v48
	v_pk_add_f32 v[50:51], v[50:51], v[90:91]
	v_add_f32_e32 v53, 1.0, v53
	v_mul_f32_e32 v54, v54, v55
	v_add_f32_e32 v48, 1.0, v48
	v_min_f32_e32 v50, 0x40e00000, v50
	v_mul_f32_e32 v53, v53, v54
	v_rcp_f32_e32 v54, v48
	v_mul_f32_e32 v48, 0x3fd9db23, v50
	v_mul_f32_e32 v48, 0xbfb8aa3b, v48
	v_exp_f32_e32 v55, v48
	v_cvt_pk_bf16_f32 v48, v52, v53
	v_med3_f32 v51, v51, s75, v170
	v_pk_add_f32 v[44:45], v[44:45], v[108:109]
	v_add_f32_e32 v53, 1.0, v55
; __device__ __forceinline__ unsigned cvt_pk_bf16(float lo, float hi) { unsigned r; asm volatile("v_cvt_pk_bf16_f32 %0, %1, %2" : "=v"(r) : "v"(lo), "v"(hi)); return r; }
; __device__ __forceinline__ float sigm(float x) { return __builtin_amdgcn_rcpf(1.0f + __expf(-x)); }
; __device__ __forceinline__ float swiglu1(float g, float l) { g = fminf(g, 7.0f); l = fminf(fmaxf(l, -7.0f), 7.0f); return g * sigm(1.702f * g) * (l + 1.0f); }
;     __device__ __forceinline__ void operator()(const f32x4 (&acc)[2][2][4][2], const Unit& u, int wr, int wc, int fr, int fq) const {
;     ...
;             for (int m = 0; m < 4; ++m) { const int row = row0 + ai * HALF + m * 16;
; #pragma unroll
;                 for (int bj = 0; bj < 2; ++bj) { const f32x4 v0 = acc[ai][bj][m][0] + bv[bj][0], v1 = acc[ai][bj][m][1] + bv[bj][1];
;                     u32x2 w; w.x = cvt_pk_bf16(swiglu1(v0[0], v0[1]), swiglu1(v0[2], v0[3])); w.y = cvt_pk_bf16(swiglu1(v1[0], v1[1]), swiglu1(v1[2], v1[3]));
;                     *(u32x2*)(O + (size_t)row * 2048 + ((col0 + bj * HALF) >> 1)) = w; } }
	v_rcp_f32_e32 v53, v53
	v_add_f32_e32 v51, 1.0, v51
	v_min_f32_e32 v44, 0x40e00000, v44
	v_med3_f32 v49, v49, s75, v170
	v_mul_f32_e32 v50, v50, v53
	v_mul_f32_e32 v50, v51, v50
	v_mul_f32_e32 v51, 0x3fd9db23, v44
	v_mul_f32_e32 v51, 0xbfb8aa3b, v51
	v_exp_f32_e32 v51, v51
	v_mul_f32_e32 v52, v56, v54
	v_add_f32_e32 v49, 1.0, v49
	v_lshl_add_u64 v[58:59], v[154:155], 0, s[46:47]
	v_mul_f32_e32 v49, v49, v52
	v_cvt_pk_bf16_f32 v49, v49, v50
	global_store_dwordx2 v[58:59], v[48:49], off offset:128 nt
	v_add_f32_e32 v48, 1.0, v51
	v_rcp_f32_e32 v48, v48
	v_pk_add_f32 v[46:47], v[46:47], v[110:111]
	v_med3_f32 v45, v45, s75, v170
	v_min_f32_e32 v46, 0x40e00000, v46
	v_mul_f32_e32 v44, v44, v48
	v_mul_f32_e32 v48, 0x3fd9db23, v46
	v_mul_f32_e32 v48, 0xbfb8aa3b, v48
	v_exp_f32_e32 v48, v48
	v_pk_add_f32 v[32:33], v[32:33], v[104:105]
	v_add_f32_e32 v45, 1.0, v45
	v_mul_f32_e32 v44, v45, v44
	v_med3_f32 v45, v47, s75, v170
	v_add_f32_e32 v47, 1.0, v48
	v_min_f32_e32 v48, 0x40e00000, v32
	v_mul_f32_e32 v32, 0x3fd9db23, v48
	v_mul_f32_e32 v32, 0xbfb8aa3b, v32
	v_rcp_f32_e32 v47, v47
	v_exp_f32_e32 v32, v32
	v_pk_add_f32 v[34:35], v[34:35], v[106:107]
	v_add_f32_e32 v45, 1.0, v45
	v_mul_f32_e32 v46, v46, v47
	v_add_f32_e32 v32, 1.0, v32
	v_min_f32_e32 v34, 0x40e00000, v34
	v_mul_f32_e32 v45, v45, v46
	v_rcp_f32_e32 v46, v32
	v_mul_f32_e32 v32, 0x3fd9db23, v34
	v_mul_f32_e32 v32, 0xbfb8aa3b, v32
	v_exp_f32_e32 v47, v32
	v_cvt_pk_bf16_f32 v32, v44, v45
	v_med3_f32 v33, v33, s75, v170
	v_pk_add_f32 v[36:37], v[36:37], v[92:93]
	v_add_f32_e32 v45, 1.0, v47
	v_mul_f32_e32 v44, v48, v46
	v_rcp_f32_e32 v45, v45
	v_add_f32_e32 v33, 1.0, v33
	v_min_f32_e32 v36, 0x40e00000, v36
	v_mul_f32_e32 v33, v33, v44
	v_mul_f32_e32 v44, 0x3fd9db23, v36
	v_mul_f32_e32 v44, 0xbfb8aa3b, v44
	v_med3_f32 v35, v35, s75, v170
	v_exp_f32_e32 v46, v44
	v_mul_f32_e32 v34, v34, v45
	v_add_f32_e32 v35, 1.0, v35
	v_add_co_u32_e32 v44, vcc, s77, v154
	v_mul_f32_e32 v34, v35, v34
	v_cvt_pk_bf16_f32 v33, v33, v34
	s_nop 0
	v_addc_co_u32_e32 v45, vcc, 0, v155, vcc
	global_store_dwordx2 v[44:45], v[32:33], off nt
	v_pk_add_f32 v[32:33], v[38:39], v[94:95]
	v_add_f32_e32 v38, 1.0, v46
	v_min_f32_e32 v32, 0x40e00000, v32
	v_rcp_f32_e32 v44, v38
	v_pk_add_f32 v[38:39], v[42:43], v[90:91]
	v_mul_f32_e32 v42, 0x3fd9db23, v32
	v_mul_f32_e32 v42, 0xbfb8aa3b, v42
	v_exp_f32_e32 v42, v42
	v_med3_f32 v37, v37, s75, v170
	v_mul_f32_e32 v36, v36, v44
	v_add_f32_e32 v37, 1.0, v37
	v_mul_f32_e32 v36, v37, v36
	v_add_f32_e32 v37, 1.0, v42
	v_rcp_f32_e32 v37, v37
	v_pk_add_f32 v[40:41], v[40:41], v[88:89]
	v_med3_f32 v33, v33, s75, v170
	v_min_f32_e32 v40, 0x40e00000, v40
	v_mul_f32_e32 v42, 0x3fd9db23, v40
	v_mul_f32_e32 v42, 0xbfb8aa3b, v42
	v_mul_f32_e32 v32, v32, v37
	v_min_f32_e32 v37, 0x40e00000, v38
	v_exp_f32_e32 v42, v42
	v_mul_f32_e32 v38, 0x3fd9db23, v37
	v_mul_f32_e32 v38, 0xbfb8aa3b, v38
	v_exp_f32_e32 v38, v38
	v_add_f32_e32 v33, 1.0, v33
	v_mul_f32_e32 v32, v33, v32
	v_add_f32_e32 v33, 1.0, v42
	v_rcp_f32_e32 v33, v33
	v_add_f32_e32 v38, 1.0, v38
	v_rcp_f32_e32 v38, v38
	v_cvt_pk_bf16_f32 v32, v36, v32
	v_med3_f32 v36, v41, s75, v170
	v_mul_f32_e32 v33, v40, v33
	v_add_f32_e32 v36, 1.0, v36
	v_mul_f32_e32 v33, v36, v33
	v_med3_f32 v36, v39, s75, v170
	v_pk_add_f32 v[20:21], v[20:21], v[108:109]
	v_mul_f32_e32 v37, v37, v38
	v_add_f32_e32 v36, 1.0, v36
	v_min_f32_e32 v20, 0x40e00000, v20
	v_mul_f32_e32 v36, v36, v37
	v_mul_f32_e32 v37, 0x3fd9db23, v20
	v_mul_f32_e32 v37, 0xbfb8aa3b, v37
	v_exp_f32_e32 v37, v37
	v_lshl_add_u64 v[34:35], v[154:155], 0, s[48:49]
	v_cvt_pk_bf16_f32 v33, v33, v36
	global_store_dwordx2 v[34:35], v[32:33], off offset:128 nt
	v_add_f32_e32 v32, 1.0, v37
	v_rcp_f32_e32 v32, v32
	v_pk_add_f32 v[22:23], v[22:23], v[110:111]
	v_med3_f32 v21, v21, s75, v170
	v_min_f32_e32 v22, 0x40e00000, v22
	v_mul_f32_e32 v20, v20, v32
	v_mul_f32_e32 v32, 0x3fd9db23, v22
	v_mul_f32_e32 v32, 0xbfb8aa3b, v32
	v_exp_f32_e32 v32, v32
	v_pk_add_f32 v[16:17], v[16:17], v[104:105]
	v_add_f32_e32 v21, 1.0, v21
	v_mul_f32_e32 v20, v21, v20
	v_med3_f32 v21, v23, s75, v170
	v_add_f32_e32 v23, 1.0, v32
	v_min_f32_e32 v32, 0x40e00000, v16
	v_mul_f32_e32 v16, 0x3fd9db23, v32
	v_mul_f32_e32 v16, 0xbfb8aa3b, v16
	v_rcp_f32_e32 v23, v23
	v_exp_f32_e32 v16, v16
	v_pk_add_f32 v[18:19], v[18:19], v[106:107]
	v_add_f32_e32 v21, 1.0, v21
	v_mul_f32_e32 v22, v22, v23
	v_add_f32_e32 v16, 1.0, v16
	v_min_f32_e32 v18, 0x40e00000, v18
	v_mul_f32_e32 v21, v21, v22
	v_rcp_f32_e32 v22, v16
	v_mul_f32_e32 v16, 0x3fd9db23, v18
	v_mul_f32_e32 v16, 0xbfb8aa3b, v16
	v_exp_f32_e32 v23, v16
	v_cvt_pk_bf16_f32 v16, v20, v21
	v_med3_f32 v17, v17, s75, v170
	v_mul_f32_e32 v20, v32, v22
	v_add_f32_e32 v21, 1.0, v23
	v_rcp_f32_e32 v21, v21
	v_add_f32_e32 v17, 1.0, v17
	v_mul_f32_e32 v17, v17, v20
	v_med3_f32 v19, v19, s75, v170
	v_mul_f32_e32 v18, v18, v21
	v_pk_add_f32 v[20:21], v[24:25], v[92:93]
; __device__ __forceinline__ unsigned cvt_pk_bf16(float lo, float hi) { unsigned r; asm volatile("v_cvt_pk_bf16_f32 %0, %1, %2" : "=v"(r) : "v"(lo), "v"(hi)); return r; }
; __device__ __forceinline__ float sigm(float x) { return __builtin_amdgcn_rcpf(1.0f + __expf(-x)); }
; __device__ __forceinline__ float swiglu1(float g, float l) { g = fminf(g, 7.0f); l = fminf(fmaxf(l, -7.0f), 7.0f); return g * sigm(1.702f * g) * (l + 1.0f); }
;     __device__ __forceinline__ void operator()(const f32x4 (&acc)[2][2][4][2], const Unit& u, int wr, int wc, int fr, int fq) const {
;     ...
;             for (int m = 0; m < 4; ++m) { const int row = row0 + ai * HALF + m * 16;
; #pragma unroll
;                 for (int bj = 0; bj < 2; ++bj) { const f32x4 v0 = acc[ai][bj][m][0] + bv[bj][0], v1 = acc[ai][bj][m][1] + bv[bj][1];
;                     u32x2 w; w.x = cvt_pk_bf16(swiglu1(v0[0], v0[1]), swiglu1(v0[2], v0[3])); w.y = cvt_pk_bf16(swiglu1(v1[0], v1[1]), swiglu1(v1[2], v1[3]));
;                     *(u32x2*)(O + (size_t)row * 2048 + ((col0 + bj * HALF) >> 1)) = w; } }
	v_add_f32_e32 v19, 1.0, v19
	v_min_f32_e32 v20, 0x40e00000, v20
	v_mul_f32_e32 v22, 0x3fd9db23, v20
	v_mul_f32_e32 v22, 0xbfb8aa3b, v22
	v_exp_f32_e32 v24, v22
	v_add_co_u32_e32 v22, vcc, s78, v154
	v_mul_f32_e32 v18, v19, v18
	s_nop 0
	v_addc_co_u32_e32 v23, vcc, 0, v155, vcc
	v_cvt_pk_bf16_f32 v17, v17, v18
	global_store_dwordx2 v[22:23], v[16:17], off nt
	v_add_f32_e32 v22, 1.0, v24
	v_pk_add_f32 v[16:17], v[26:27], v[94:95]
	v_rcp_f32_e32 v26, v22
	v_min_f32_e32 v16, 0x40e00000, v16
	v_med3_f32 v21, v21, s75, v170
	v_add_f32_e32 v21, 1.0, v21
	v_mul_f32_e32 v20, v20, v26
	v_mul_f32_e32 v26, 0x3fd9db23, v16
	v_mul_f32_e32 v26, 0xbfb8aa3b, v26
	v_exp_f32_e32 v26, v26
	v_mul_f32_e32 v20, v21, v20
	v_pk_add_f32 v[24:25], v[28:29], v[88:89]
	v_pk_add_f32 v[22:23], v[30:31], v[90:91]
	v_add_f32_e32 v21, 1.0, v26
	v_rcp_f32_e32 v21, v21
	v_min_f32_e32 v24, 0x40e00000, v24
	v_mul_f32_e32 v26, 0x3fd9db23, v24
	v_mul_f32_e32 v26, 0xbfb8aa3b, v26
	v_mul_f32_e32 v16, v16, v21
	v_min_f32_e32 v21, 0x40e00000, v22
	v_exp_f32_e32 v26, v26
	v_mul_f32_e32 v22, 0x3fd9db23, v21
	v_mul_f32_e32 v22, 0xbfb8aa3b, v22
	v_med3_f32 v17, v17, s75, v170
	v_exp_f32_e32 v22, v22
	v_add_f32_e32 v17, 1.0, v17
	v_mul_f32_e32 v16, v17, v16
	v_add_f32_e32 v17, 1.0, v26
	v_rcp_f32_e32 v17, v17
	v_add_f32_e32 v22, 1.0, v22
	v_rcp_f32_e32 v22, v22
	v_cvt_pk_bf16_f32 v16, v20, v16
	v_med3_f32 v20, v25, s75, v170
	v_mul_f32_e32 v17, v24, v17
	v_add_f32_e32 v20, 1.0, v20
	v_mul_f32_e32 v17, v20, v17
	v_med3_f32 v20, v23, s75, v170
	v_pk_add_f32 v[4:5], v[4:5], v[108:109]
	v_mul_f32_e32 v21, v21, v22
	v_add_f32_e32 v20, 1.0, v20
	v_min_f32_e32 v4, 0x40e00000, v4
	v_mul_f32_e32 v20, v20, v21
	v_mul_f32_e32 v21, 0x3fd9db23, v4
	v_mul_f32_e32 v21, 0xbfb8aa3b, v21
	v_exp_f32_e32 v21, v21
	v_lshl_add_u64 v[18:19], v[154:155], 0, s[50:51]
	v_cvt_pk_bf16_f32 v17, v17, v20
	global_store_dwordx2 v[18:19], v[16:17], off offset:128 nt
	v_add_f32_e32 v16, 1.0, v21
	v_rcp_f32_e32 v16, v16
	v_pk_add_f32 v[6:7], v[6:7], v[110:111]
	v_med3_f32 v5, v5, s75, v170
	v_min_f32_e32 v6, 0x40e00000, v6
	v_mul_f32_e32 v4, v4, v16
	v_mul_f32_e32 v16, 0x3fd9db23, v6
	v_mul_f32_e32 v16, 0xbfb8aa3b, v16
	v_exp_f32_e32 v16, v16
	v_pk_add_f32 v[0:1], v[0:1], v[104:105]
	v_add_f32_e32 v5, 1.0, v5
	v_mul_f32_e32 v4, v5, v4
	v_med3_f32 v5, v7, s75, v170
	v_add_f32_e32 v7, 1.0, v16
	v_min_f32_e32 v16, 0x40e00000, v0
	v_mul_f32_e32 v0, 0x3fd9db23, v16
	v_mul_f32_e32 v0, 0xbfb8aa3b, v0
	v_rcp_f32_e32 v7, v7
	v_exp_f32_e32 v0, v0
	v_pk_add_f32 v[2:3], v[2:3], v[106:107]
	v_add_f32_e32 v5, 1.0, v5
	v_mul_f32_e32 v6, v6, v7
	v_add_f32_e32 v0, 1.0, v0
	v_min_f32_e32 v2, 0x40e00000, v2
	v_mul_f32_e32 v5, v5, v6
	v_rcp_f32_e32 v6, v0
	v_mul_f32_e32 v0, 0x3fd9db23, v2
	v_mul_f32_e32 v0, 0xbfb8aa3b, v0
	v_exp_f32_e32 v7, v0
	v_cvt_pk_bf16_f32 v0, v4, v5
	v_med3_f32 v1, v1, s75, v170
	v_mul_f32_e32 v4, v16, v6
	v_add_f32_e32 v5, 1.0, v7
	v_rcp_f32_e32 v5, v5
	v_add_f32_e32 v1, 1.0, v1
	v_mul_f32_e32 v1, v1, v4
	v_med3_f32 v3, v3, s75, v170
	v_mul_f32_e32 v2, v2, v5
	v_pk_add_f32 v[4:5], v[8:9], v[92:93]
	v_add_f32_e32 v3, 1.0, v3
	v_min_f32_e32 v4, 0x40e00000, v4
	v_mul_f32_e32 v6, 0x3fd9db23, v4
	v_mul_f32_e32 v6, 0xbfb8aa3b, v6
	v_exp_f32_e32 v8, v6
	v_add_co_u32_e32 v6, vcc, s79, v154
	v_mul_f32_e32 v2, v3, v2
	s_nop 0
	v_addc_co_u32_e32 v7, vcc, 0, v155, vcc
	v_cvt_pk_bf16_f32 v1, v1, v2
	global_store_dwordx2 v[6:7], v[0:1], off nt
	v_add_f32_e32 v6, 1.0, v8
	v_pk_add_f32 v[0:1], v[10:11], v[94:95]
	v_rcp_f32_e32 v10, v6
	v_min_f32_e32 v0, 0x40e00000, v0
	v_med3_f32 v5, v5, s75, v170
	v_add_f32_e32 v5, 1.0, v5
	v_mul_f32_e32 v4, v4, v10
	v_mul_f32_e32 v10, 0x3fd9db23, v0
	v_mul_f32_e32 v10, 0xbfb8aa3b, v10
	v_exp_f32_e32 v10, v10
	v_mul_f32_e32 v4, v5, v4
	v_pk_add_f32 v[8:9], v[12:13], v[88:89]
	v_pk_add_f32 v[6:7], v[14:15], v[90:91]
	v_add_f32_e32 v5, 1.0, v10
	v_rcp_f32_e32 v5, v5
	v_min_f32_e32 v8, 0x40e00000, v8
	v_mul_f32_e32 v10, 0x3fd9db23, v8
	v_mul_f32_e32 v10, 0xbfb8aa3b, v10
	v_mul_f32_e32 v0, v0, v5
	v_min_f32_e32 v5, 0x40e00000, v6
	v_exp_f32_e32 v10, v10
	v_mul_f32_e32 v6, 0x3fd9db23, v5
	v_mul_f32_e32 v6, 0xbfb8aa3b, v6
	v_med3_f32 v1, v1, s75, v170
	v_exp_f32_e32 v6, v6
	v_add_f32_e32 v1, 1.0, v1
	v_mul_f32_e32 v0, v1, v0
	v_add_f32_e32 v1, 1.0, v10
	v_rcp_f32_e32 v1, v1
	v_add_f32_e32 v6, 1.0, v6
	v_rcp_f32_e32 v6, v6
	v_cvt_pk_bf16_f32 v0, v4, v0
	v_med3_f32 v4, v9, s75, v170
	v_mul_f32_e32 v1, v8, v1
	v_add_f32_e32 v4, 1.0, v4
	v_mul_f32_e32 v1, v4, v1
	v_med3_f32 v4, v7, s75, v170
	v_lshl_add_u64 v[2:3], v[154:155], 0, s[52:53]
	v_mul_f32_e32 v5, v5, v6
	v_add_f32_e32 v4, 1.0, v4
	s_and_b64 vcc, exec, s[2:3]
	s_mov_b64 s[2:3], -1
	v_mul_f32_e32 v4, v4, v5
	v_cvt_pk_bf16_f32 v1, v1, v4
	global_store_dwordx2 v[2:3], v[0:1], off offset:128 nt
	s_cbranch_vccnz .LBB0_2196
	s_andn2_b64 vcc, exec, s[30:31]
	s_cbranch_vccnz .LBB0_2195
	s_barrier
	s_branch .LBB0_2195

; __device__ __forceinline__ unsigned cvt_pk_bf16(float lo, float hi) { unsigned r; asm volatile("v_cvt_pk_bf16_f32 %0, %1, %2" : "=v"(r) : "v"(lo), "v"(hi)); return r; }
; __device__ __forceinline__ float sigm(float x) { return __builtin_amdgcn_rcpf(1.0f + __expf(-x)); }
; __device__ __forceinline__ float swiglu1(float g, float l) { g = fminf(g, 7.0f); l = fminf(fmaxf(l, -7.0f), 7.0f); return g * sigm(1.702f * g) * (l + 1.0f); }
;     __device__ __forceinline__ void operator()(const f32x4 (&acc)[2][2][4][2], const Unit& u, int wr, int wc, int fr, int fq) const {
;         const int row0 = u.pm * BM + wr * 64 + fr, col0 = u.pn * BM + wc * 32 + 8 * fq; const float* bb = bias + (size_t)u.e * 4096;
;         f32x4 bv[2][2];
; #pragma unroll
;         for (int bj = 0; bj < 2; ++bj)
; #pragma unroll
;             for (int n = 0; n < 2; ++n) bv[bj][n] = *(const f32x4*)(bb + col0 + bj * HALF + 4 * n);
; #pragma unroll
;         for (int ai = 0; ai < 2; ++ai)
; #pragma unroll
;             for (int m = 0; m < 4; ++m) { const int row = row0 + ai * HALF + m * 16;
; #pragma unroll
;                 for (int bj = 0; bj < 2; ++bj) { const f32x4 v0 = acc[ai][bj][m][0] + bv[bj][0], v1 = acc[ai][bj][m][1] + bv[bj][1];
;                     u32x2 w; w.x = cvt_pk_bf16(swiglu1(v0[0], v0[1]), swiglu1(v0[2], v0[3])); w.y = cvt_pk_bf16(swiglu1(v1[0], v1[1]), swiglu1(v1[2], v1[3]));
;                     *(u32x2*)(O + (size_t)row * 2048 + ((col0 + bj * HALF) >> 1)) = w; } }
.LBB0_2303:
	v_ashrrev_i32_e32 v89, 31, v88
	v_lshl_or_b32 v154, s56, 8, v166
	v_lshlrev_b64 v[88:89], 14, v[88:89]
	v_lshl_add_u64 v[88:89], s[12:13], 0, v[88:89]
	v_ashrrev_i32_e32 v155, 31, v154
	v_lshl_add_u64 v[88:89], v[154:155], 2, v[88:89]
	global_load_dwordx4 v[108:111], v[88:89], off
	global_load_dwordx4 v[104:107], v[88:89], off offset:16
	global_load_dwordx4 v[92:95], v[88:89], off offset:512
	s_nop 0
	global_load_dwordx4 v[88:91], v[88:89], off offset:528
	v_lshl_add_u32 v158, s5, 8, v164
	v_ashrrev_i32_e32 v159, 31, v158
	v_ashrrev_i32_e32 v154, 1, v154
	v_lshlrev_b64 v[156:157], 12, v[158:159]
	v_ashrrev_i32_e32 v155, 31, v154
	v_lshl_add_u64 v[176:177], s[26:27], 0, v[156:157]
	v_lshlrev_b64 v[156:157], 1, v[154:155]
	v_lshl_add_u64 v[154:155], v[176:177], 0, v[156:157]
	s_waitcnt vmcnt(0)
	v_pk_add_f32 v[140:141], v[140:141], v[108:109]
	v_pk_add_f32 v[142:143], v[142:143], v[110:111]
	v_pk_add_f32 v[132:133], v[132:133], v[92:93]
	v_pk_add_f32 v[128:129], v[128:129], v[88:89]
	v_min_f32_e32 v140, 0x40e00000, v140
	v_pk_add_f32 v[138:139], v[138:139], v[106:107]
	v_pk_add_f32 v[136:137], v[136:137], v[104:105]
	v_pk_add_f32 v[134:135], v[134:135], v[94:95]
	v_med3_f32 v141, v141, s74, v170
	v_min_f32_e32 v142, 0x40e00000, v142
	v_min_f32_e32 v132, 0x40e00000, v132
	v_min_f32_e32 v148, 0x40e00000, v128
	v_mul_f32_e32 v128, 0x3fd9db23, v140
	v_min_f32_e32 v136, 0x40e00000, v136
	v_min_f32_e32 v138, 0x40e00000, v138
	v_min_f32_e32 v134, 0x40e00000, v134
	v_med3_f32 v151, v129, s74, v170
	v_add_f32_e32 v129, 1.0, v141
	v_mul_f32_e32 v141, 0x3fd9db23, v142
	v_mul_f32_e32 v176, 0x3fd9db23, v132
	v_mul_f32_e32 v128, 0xbfb8aa3b, v128
	v_mul_f32_e32 v159, 0x3fd9db23, v136
	v_mul_f32_e32 v175, 0x3fd9db23, v138
	v_mul_f32_e32 v177, 0x3fd9db23, v134
	v_mul_f32_e32 v141, 0xbfb8aa3b, v141
	v_mul_f32_e32 v176, 0xbfb8aa3b, v176
	v_exp_f32_e32 v128, v128
	v_mul_f32_e32 v159, 0xbfb8aa3b, v159
	v_mul_f32_e32 v175, 0xbfb8aa3b, v175
	v_mul_f32_e32 v177, 0xbfb8aa3b, v177
	v_exp_f32_e32 v141, v141
	v_exp_f32_e32 v176, v176
	v_exp_f32_e32 v159, v159
	v_exp_f32_e32 v175, v175
	v_exp_f32_e32 v177, v177
	v_pk_add_f32 v[130:131], v[130:131], v[90:91]
	v_add_f32_e32 v128, 1.0, v128
	v_min_f32_e32 v130, 0x40e00000, v130
	v_mul_f32_e32 v178, 0x3fd9db23, v148
	v_add_f32_e32 v141, 1.0, v141
	v_add_f32_e32 v176, 1.0, v176
	v_rcp_f32_e32 v128, v128
	v_mul_f32_e32 v179, 0x3fd9db23, v130
	v_mul_f32_e32 v178, 0xbfb8aa3b, v178
	v_add_f32_e32 v159, 1.0, v159
	v_add_f32_e32 v175, 1.0, v175
	v_add_f32_e32 v177, 1.0, v177
	v_rcp_f32_e32 v141, v141
	v_rcp_f32_e32 v176, v176
	v_mul_f32_e32 v179, 0xbfb8aa3b, v179
	v_exp_f32_e32 v178, v178
	v_rcp_f32_e32 v159, v159
	v_rcp_f32_e32 v175, v175
	v_rcp_f32_e32 v177, v177
	v_exp_f32_e32 v179, v179
	v_med3_f32 v143, v143, s74, v170
	v_med3_f32 v133, v133, s74, v170
	v_mul_f32_e32 v128, v140, v128
	v_med3_f32 v137, v137, s74, v170
	v_med3_f32 v139, v139, s74, v170
	v_med3_f32 v135, v135, s74, v170
	v_add_f32_e32 v143, 1.0, v143
	v_add_f32_e32 v133, 1.0, v133
	v_mul_f32_e32 v140, v142, v141
	v_mul_f32_e32 v132, v132, v176
	v_mul_f32_e32 v128, v129, v128
	v_add_f32_e32 v137, 1.0, v137
	v_add_f32_e32 v139, 1.0, v139
	v_add_f32_e32 v135, 1.0, v135
	v_add_f32_e32 v178, 1.0, v178
	v_mul_f32_e32 v136, v136, v159
	v_mul_f32_e32 v138, v138, v175
	v_mul_f32_e32 v134, v134, v177
	v_mul_f32_e32 v129, v143, v140
	v_mul_f32_e32 v132, v133, v132
	v_cvt_pk_bf16_f32 v128, v128, v129
	v_rcp_f32_e32 v178, v178
	v_mul_f32_e32 v136, v137, v136
	v_mul_f32_e32 v137, v139, v138
	v_mul_f32_e32 v133, v135, v134
	v_cvt_pk_bf16_f32 v129, v136, v137
	global_store_dwordx2 v[154:155], v[128:129], off nt
	v_cvt_pk_bf16_f32 v128, v132, v133
	v_add_f32_e32 v132, 1.0, v179
	v_rcp_f32_e32 v132, v132
	v_mul_f32_e32 v129, v148, v178
	v_add_f32_e32 v133, 1.0, v151
	v_med3_f32 v131, v131, s74, v170
	v_mul_f32_e32 v129, v133, v129
	v_mul_f32_e32 v130, v130, v132
	v_add_f32_e32 v131, 1.0, v131
	v_pk_add_f32 v[124:125], v[124:125], v[108:109]
	v_mul_f32_e32 v130, v131, v130
	v_cvt_pk_bf16_f32 v129, v129, v130
	v_min_f32_e32 v124, 0x40e00000, v124
	global_store_dwordx2 v[154:155], v[128:129], off offset:128 nt
	v_mul_f32_e32 v129, 0x3fd9db23, v124
	v_mul_f32_e32 v129, 0xbfb8aa3b, v129
	v_exp_f32_e32 v130, v129
	v_pk_add_f32 v[126:127], v[126:127], v[110:111]
	v_med3_f32 v125, v125, s74, v170
	v_min_f32_e32 v126, 0x40e00000, v126
	v_add_f32_e32 v130, 1.0, v130
	v_rcp_f32_e32 v130, v130
	v_pk_add_f32 v[120:121], v[120:121], v[104:105]
	v_add_f32_e32 v125, 1.0, v125
	v_pk_add_f32 v[122:123], v[122:123], v[106:107]
	v_mul_f32_e32 v124, v124, v130
	v_mul_f32_e32 v130, 0x3fd9db23, v126
	v_mul_f32_e32 v130, 0xbfb8aa3b, v130
	v_exp_f32_e32 v130, v130
	v_mul_f32_e32 v124, v125, v124
	v_med3_f32 v125, v127, s74, v170
	v_add_f32_e32 v125, 1.0, v125
	v_add_f32_e32 v127, 1.0, v130
	v_min_f32_e32 v130, 0x40e00000, v120
	v_mul_f32_e32 v120, 0x3fd9db23, v130
	v_mul_f32_e32 v120, 0xbfb8aa3b, v120
	v_rcp_f32_e32 v127, v127
	v_exp_f32_e32 v120, v120
	v_min_f32_e32 v122, 0x40e00000, v122
	v_med3_f32 v121, v121, s74, v170
	v_mul_f32_e32 v126, v126, v127
	v_add_f32_e32 v120, 1.0, v120
	v_mul_f32_e32 v125, v125, v126
	v_rcp_f32_e32 v126, v120
	v_mul_f32_e32 v120, 0x3fd9db23, v122
	v_mul_f32_e32 v120, 0xbfb8aa3b, v120
	v_exp_f32_e32 v127, v120
	v_cvt_pk_bf16_f32 v120, v124, v125
	v_pk_add_f32 v[116:117], v[116:117], v[92:93]
	v_mul_f32_e32 v124, v130, v126
	v_add_f32_e32 v125, 1.0, v127
	v_rcp_f32_e32 v125, v125
	v_add_f32_e32 v121, 1.0, v121
	v_min_f32_e32 v116, 0x40e00000, v116
	v_mul_f32_e32 v121, v121, v124
	v_mul_f32_e32 v124, 0x3fd9db23, v116
	v_or_b32_e32 v128, 16, v158
; __device__ __forceinline__ unsigned cvt_pk_bf16(float lo, float hi) { unsigned r; asm volatile("v_cvt_pk_bf16_f32 %0, %1, %2" : "=v"(r) : "v"(lo), "v"(hi)); return r; }
; __device__ __forceinline__ float sigm(float x) { return __builtin_amdgcn_rcpf(1.0f + __expf(-x)); }
; __device__ __forceinline__ float swiglu1(float g, float l) { g = fminf(g, 7.0f); l = fminf(fmaxf(l, -7.0f), 7.0f); return g * sigm(1.702f * g) * (l + 1.0f); }
;     __device__ __forceinline__ void operator()(const f32x4 (&acc)[2][2][4][2], const Unit& u, int wr, int wc, int fr, int fq) const {
;     ...
;             for (int m = 0; m < 4; ++m) { const int row = row0 + ai * HALF + m * 16;
; #pragma unroll
;                 for (int bj = 0; bj < 2; ++bj) { const f32x4 v0 = acc[ai][bj][m][0] + bv[bj][0], v1 = acc[ai][bj][m][1] + bv[bj][1];
;                     u32x2 w; w.x = cvt_pk_bf16(swiglu1(v0[0], v0[1]), swiglu1(v0[2], v0[3])); w.y = cvt_pk_bf16(swiglu1(v1[0], v1[1]), swiglu1(v1[2], v1[3]));
;                     *(u32x2*)(O + (size_t)row * 2048 + ((col0 + bj * HALF) >> 1)) = w; } }
	v_med3_f32 v123, v123, s74, v170
	v_mul_f32_e32 v124, 0xbfb8aa3b, v124
	v_ashrrev_i32_e32 v129, 31, v128
	v_mul_f32_e32 v122, v122, v125
	v_add_f32_e32 v123, 1.0, v123
	v_exp_f32_e32 v124, v124
	v_lshlrev_b64 v[128:129], 12, v[128:129]
	v_mul_f32_e32 v122, v123, v122
	v_cvt_pk_bf16_f32 v121, v121, v122
	v_lshl_add_u64 v[122:123], s[26:27], 0, v[128:129]
	v_lshl_add_u64 v[122:123], v[122:123], 0, v[156:157]
	global_store_dwordx2 v[122:123], v[120:121], off nt
	v_add_f32_e32 v120, 1.0, v124
	v_rcp_f32_e32 v120, v120
	v_pk_add_f32 v[118:119], v[118:119], v[94:95]
	v_med3_f32 v117, v117, s74, v170
	v_min_f32_e32 v118, 0x40e00000, v118
	v_mul_f32_e32 v116, v116, v120
	v_mul_f32_e32 v120, 0x3fd9db23, v118
	v_mul_f32_e32 v120, 0xbfb8aa3b, v120
	v_exp_f32_e32 v120, v120
	v_pk_add_f32 v[112:113], v[112:113], v[88:89]
	v_add_f32_e32 v117, 1.0, v117
	v_mul_f32_e32 v116, v117, v116
	v_med3_f32 v117, v119, s74, v170
	v_add_f32_e32 v119, 1.0, v120
	v_min_f32_e32 v120, 0x40e00000, v112
	v_mul_f32_e32 v112, 0x3fd9db23, v120
	v_mul_f32_e32 v112, 0xbfb8aa3b, v112
	v_rcp_f32_e32 v119, v119
	v_exp_f32_e32 v112, v112
	v_pk_add_f32 v[114:115], v[114:115], v[90:91]
	v_add_f32_e32 v117, 1.0, v117
	v_mul_f32_e32 v118, v118, v119
	v_add_f32_e32 v112, 1.0, v112
	v_min_f32_e32 v114, 0x40e00000, v114
	v_mul_f32_e32 v117, v117, v118
	v_rcp_f32_e32 v118, v112
	v_mul_f32_e32 v112, 0x3fd9db23, v114
	v_mul_f32_e32 v112, 0xbfb8aa3b, v112
	v_exp_f32_e32 v119, v112
	v_cvt_pk_bf16_f32 v112, v116, v117
	v_med3_f32 v113, v113, s74, v170
	v_mul_f32_e32 v116, v120, v118
	v_add_f32_e32 v117, 1.0, v119
	v_rcp_f32_e32 v117, v117
	v_add_f32_e32 v113, 1.0, v113
	v_med3_f32 v115, v115, s74, v170
	v_mul_f32_e32 v113, v113, v116
	v_mul_f32_e32 v114, v114, v117
	v_add_f32_e32 v115, 1.0, v115
	v_pk_add_f32 v[100:101], v[100:101], v[108:109]
	v_mul_f32_e32 v114, v115, v114
	v_cvt_pk_bf16_f32 v113, v113, v114
	v_min_f32_e32 v100, 0x40e00000, v100
	global_store_dwordx2 v[122:123], v[112:113], off offset:128 nt
	v_mul_f32_e32 v113, 0x3fd9db23, v100
	v_mul_f32_e32 v113, 0xbfb8aa3b, v113
	v_exp_f32_e32 v114, v113
	v_pk_add_f32 v[102:103], v[102:103], v[110:111]
	v_med3_f32 v101, v101, s74, v170
	v_min_f32_e32 v102, 0x40e00000, v102
	v_add_f32_e32 v114, 1.0, v114
	v_rcp_f32_e32 v114, v114
	v_pk_add_f32 v[96:97], v[96:97], v[104:105]
	v_add_f32_e32 v101, 1.0, v101
	v_pk_add_f32 v[98:99], v[98:99], v[106:107]
	v_mul_f32_e32 v100, v100, v114
	v_mul_f32_e32 v114, 0x3fd9db23, v102
	v_mul_f32_e32 v114, 0xbfb8aa3b, v114
	v_exp_f32_e32 v114, v114
	v_mul_f32_e32 v100, v101, v100
	v_med3_f32 v101, v103, s74, v170
	v_add_f32_e32 v101, 1.0, v101
	v_add_f32_e32 v103, 1.0, v114
	v_min_f32_e32 v114, 0x40e00000, v96
	v_mul_f32_e32 v96, 0x3fd9db23, v114
	v_mul_f32_e32 v96, 0xbfb8aa3b, v96
	v_rcp_f32_e32 v103, v103
	v_exp_f32_e32 v96, v96
	v_min_f32_e32 v98, 0x40e00000, v98
	v_med3_f32 v97, v97, s74, v170
	v_mul_f32_e32 v102, v102, v103
	v_add_f32_e32 v96, 1.0, v96
	v_mul_f32_e32 v101, v101, v102
	v_rcp_f32_e32 v102, v96
	v_mul_f32_e32 v96, 0x3fd9db23, v98
	v_mul_f32_e32 v96, 0xbfb8aa3b, v96
	v_exp_f32_e32 v103, v96
	v_cvt_pk_bf16_f32 v96, v100, v101
	v_pk_add_f32 v[84:85], v[84:85], v[92:93]
	v_mul_f32_e32 v100, v114, v102
	v_add_f32_e32 v101, 1.0, v103
	v_rcp_f32_e32 v101, v101
	v_add_f32_e32 v97, 1.0, v97
	v_min_f32_e32 v84, 0x40e00000, v84
	v_mul_f32_e32 v97, v97, v100
	v_mul_f32_e32 v100, 0x3fd9db23, v84
	v_or_b32_e32 v112, 32, v158
	v_med3_f32 v99, v99, s74, v170
	v_mul_f32_e32 v100, 0xbfb8aa3b, v100
	v_ashrrev_i32_e32 v113, 31, v112
	v_mul_f32_e32 v98, v98, v101
	v_add_f32_e32 v99, 1.0, v99
	v_exp_f32_e32 v100, v100
	v_lshlrev_b64 v[112:113], 12, v[112:113]
	v_mul_f32_e32 v98, v99, v98
	v_cvt_pk_bf16_f32 v97, v97, v98
	v_lshl_add_u64 v[98:99], s[26:27], 0, v[112:113]
	v_lshl_add_u64 v[98:99], v[98:99], 0, v[156:157]
	global_store_dwordx2 v[98:99], v[96:97], off nt
	v_add_f32_e32 v96, 1.0, v100
	v_rcp_f32_e32 v96, v96
	v_pk_add_f32 v[86:87], v[86:87], v[94:95]
	v_med3_f32 v85, v85, s74, v170
	v_min_f32_e32 v86, 0x40e00000, v86
	v_mul_f32_e32 v84, v84, v96
	v_mul_f32_e32 v96, 0x3fd9db23, v86
	v_mul_f32_e32 v96, 0xbfb8aa3b, v96
	v_exp_f32_e32 v96, v96
	v_pk_add_f32 v[80:81], v[80:81], v[88:89]
	v_add_f32_e32 v85, 1.0, v85
	v_mul_f32_e32 v84, v85, v84
	v_med3_f32 v85, v87, s74, v170
	v_add_f32_e32 v87, 1.0, v96
	v_min_f32_e32 v96, 0x40e00000, v80
	v_mul_f32_e32 v80, 0x3fd9db23, v96
	v_mul_f32_e32 v80, 0xbfb8aa3b, v80
	v_rcp_f32_e32 v87, v87
	v_exp_f32_e32 v80, v80
	v_pk_add_f32 v[82:83], v[82:83], v[90:91]
	v_add_f32_e32 v85, 1.0, v85
	v_mul_f32_e32 v86, v86, v87
	v_add_f32_e32 v80, 1.0, v80
	v_min_f32_e32 v82, 0x40e00000, v82
	v_mul_f32_e32 v85, v85, v86
	v_rcp_f32_e32 v86, v80
	v_mul_f32_e32 v80, 0x3fd9db23, v82
	v_mul_f32_e32 v80, 0xbfb8aa3b, v80
	v_exp_f32_e32 v87, v80
	v_cvt_pk_bf16_f32 v80, v84, v85
	v_med3_f32 v81, v81, s74, v170
	v_mul_f32_e32 v84, v96, v86
	v_add_f32_e32 v85, 1.0, v87
	v_rcp_f32_e32 v85, v85
	v_add_f32_e32 v81, 1.0, v81
	v_med3_f32 v83, v83, s74, v170
	v_mul_f32_e32 v81, v81, v84
	v_mul_f32_e32 v82, v82, v85
	v_add_f32_e32 v83, 1.0, v83
	v_pk_add_f32 v[76:77], v[76:77], v[108:109]
	v_mul_f32_e32 v82, v83, v82
	v_cvt_pk_bf16_f32 v81, v81, v82
	v_min_f32_e32 v76, 0x40e00000, v76
	global_store_dwordx2 v[98:99], v[80:81], off offset:128 nt
	v_mul_f32_e32 v81, 0x3fd9db23, v76
	v_mul_f32_e32 v81, 0xbfb8aa3b, v81
	v_exp_f32_e32 v82, v81
	v_pk_add_f32 v[78:79], v[78:79], v[110:111]
	v_med3_f32 v77, v77, s74, v170
	v_min_f32_e32 v78, 0x40e00000, v78
	v_add_f32_e32 v82, 1.0, v82
	v_rcp_f32_e32 v82, v82
	v_pk_add_f32 v[72:73], v[72:73], v[104:105]
	v_add_f32_e32 v77, 1.0, v77
; __device__ __forceinline__ unsigned cvt_pk_bf16(float lo, float hi) { unsigned r; asm volatile("v_cvt_pk_bf16_f32 %0, %1, %2" : "=v"(r) : "v"(lo), "v"(hi)); return r; }
; __device__ __forceinline__ float sigm(float x) { return __builtin_amdgcn_rcpf(1.0f + __expf(-x)); }
; __device__ __forceinline__ float swiglu1(float g, float l) { g = fminf(g, 7.0f); l = fminf(fmaxf(l, -7.0f), 7.0f); return g * sigm(1.702f * g) * (l + 1.0f); }
;     __device__ __forceinline__ void operator()(const f32x4 (&acc)[2][2][4][2], const Unit& u, int wr, int wc, int fr, int fq) const {
;     ...
;             for (int m = 0; m < 4; ++m) { const int row = row0 + ai * HALF + m * 16;
; #pragma unroll
;                 for (int bj = 0; bj < 2; ++bj) { const f32x4 v0 = acc[ai][bj][m][0] + bv[bj][0], v1 = acc[ai][bj][m][1] + bv[bj][1];
;                     u32x2 w; w.x = cvt_pk_bf16(swiglu1(v0[0], v0[1]), swiglu1(v0[2], v0[3])); w.y = cvt_pk_bf16(swiglu1(v1[0], v1[1]), swiglu1(v1[2], v1[3]));
;                     *(u32x2*)(O + (size_t)row * 2048 + ((col0 + bj * HALF) >> 1)) = w; } }
	v_pk_add_f32 v[74:75], v[74:75], v[106:107]
	v_mul_f32_e32 v76, v76, v82
	v_mul_f32_e32 v82, 0x3fd9db23, v78
	v_mul_f32_e32 v82, 0xbfb8aa3b, v82
	v_exp_f32_e32 v82, v82
	v_mul_f32_e32 v76, v77, v76
	v_med3_f32 v77, v79, s74, v170
	v_add_f32_e32 v77, 1.0, v77
	v_add_f32_e32 v79, 1.0, v82
	v_min_f32_e32 v82, 0x40e00000, v72
	v_mul_f32_e32 v72, 0x3fd9db23, v82
	v_mul_f32_e32 v72, 0xbfb8aa3b, v72
	v_rcp_f32_e32 v79, v79
	v_exp_f32_e32 v72, v72
	v_min_f32_e32 v74, 0x40e00000, v74
	v_med3_f32 v73, v73, s74, v170
	v_mul_f32_e32 v78, v78, v79
	v_add_f32_e32 v72, 1.0, v72
	v_mul_f32_e32 v77, v77, v78
	v_rcp_f32_e32 v78, v72
	v_mul_f32_e32 v72, 0x3fd9db23, v74
	v_mul_f32_e32 v72, 0xbfb8aa3b, v72
	v_exp_f32_e32 v79, v72
	v_cvt_pk_bf16_f32 v72, v76, v77
	v_pk_add_f32 v[68:69], v[68:69], v[92:93]
	v_mul_f32_e32 v76, v82, v78
	v_add_f32_e32 v77, 1.0, v79
	v_rcp_f32_e32 v77, v77
	v_add_f32_e32 v73, 1.0, v73
	v_min_f32_e32 v68, 0x40e00000, v68
	v_mul_f32_e32 v73, v73, v76
	v_mul_f32_e32 v76, 0x3fd9db23, v68
	v_or_b32_e32 v80, 48, v158
	v_med3_f32 v75, v75, s74, v170
	v_mul_f32_e32 v76, 0xbfb8aa3b, v76
	v_ashrrev_i32_e32 v81, 31, v80
	v_mul_f32_e32 v74, v74, v77
	v_add_f32_e32 v75, 1.0, v75
	v_exp_f32_e32 v76, v76
	v_lshlrev_b64 v[80:81], 12, v[80:81]
	v_mul_f32_e32 v74, v75, v74
	v_cvt_pk_bf16_f32 v73, v73, v74
	v_lshl_add_u64 v[74:75], s[26:27], 0, v[80:81]
	v_lshl_add_u64 v[74:75], v[74:75], 0, v[156:157]
	global_store_dwordx2 v[74:75], v[72:73], off nt
	v_add_f32_e32 v72, 1.0, v76
	v_rcp_f32_e32 v72, v72
	v_pk_add_f32 v[70:71], v[70:71], v[94:95]
	v_med3_f32 v69, v69, s74, v170
	v_min_f32_e32 v70, 0x40e00000, v70
	v_mul_f32_e32 v68, v68, v72
	v_mul_f32_e32 v72, 0x3fd9db23, v70
	v_mul_f32_e32 v72, 0xbfb8aa3b, v72
	v_exp_f32_e32 v72, v72
	v_pk_add_f32 v[64:65], v[64:65], v[88:89]
	v_add_f32_e32 v69, 1.0, v69
	v_mul_f32_e32 v68, v69, v68
	v_med3_f32 v69, v71, s74, v170
	v_add_f32_e32 v71, 1.0, v72
	v_min_f32_e32 v72, 0x40e00000, v64
	v_mul_f32_e32 v64, 0x3fd9db23, v72
	v_mul_f32_e32 v64, 0xbfb8aa3b, v64
	v_rcp_f32_e32 v71, v71
	v_exp_f32_e32 v64, v64
	v_pk_add_f32 v[66:67], v[66:67], v[90:91]
	v_add_f32_e32 v69, 1.0, v69
	v_mul_f32_e32 v70, v70, v71
	v_add_f32_e32 v64, 1.0, v64
	v_min_f32_e32 v66, 0x40e00000, v66
	v_mul_f32_e32 v69, v69, v70
	v_rcp_f32_e32 v70, v64
	v_mul_f32_e32 v64, 0x3fd9db23, v66
	v_mul_f32_e32 v64, 0xbfb8aa3b, v64
	v_exp_f32_e32 v71, v64
	v_cvt_pk_bf16_f32 v64, v68, v69
	v_med3_f32 v67, v67, s74, v170
	v_pk_add_f32 v[60:61], v[60:61], v[108:109]
	v_add_f32_e32 v69, 1.0, v71
	v_rcp_f32_e32 v69, v69
	v_add_f32_e32 v67, 1.0, v67
	v_min_f32_e32 v60, 0x40e00000, v60
	v_med3_f32 v65, v65, s74, v170
	v_mul_f32_e32 v66, v66, v69
	v_mul_f32_e32 v66, v67, v66
	v_mul_f32_e32 v67, 0x3fd9db23, v60
	v_mul_f32_e32 v67, 0xbfb8aa3b, v67
	v_exp_f32_e32 v67, v67
	v_mul_f32_e32 v68, v72, v70
	v_add_f32_e32 v65, 1.0, v65
	v_mul_f32_e32 v65, v65, v68
	v_cvt_pk_bf16_f32 v65, v65, v66
	global_store_dwordx2 v[74:75], v[64:65], off offset:128 nt
	v_add_f32_e32 v64, 1.0, v67
	v_rcp_f32_e32 v64, v64
	v_pk_add_f32 v[62:63], v[62:63], v[110:111]
	v_med3_f32 v61, v61, s74, v170
	v_min_f32_e32 v62, 0x40e00000, v62
	v_mul_f32_e32 v60, v60, v64
	v_mul_f32_e32 v64, 0x3fd9db23, v62
	v_mul_f32_e32 v64, 0xbfb8aa3b, v64
	v_exp_f32_e32 v64, v64
	v_pk_add_f32 v[56:57], v[56:57], v[104:105]
	v_add_f32_e32 v61, 1.0, v61
	v_mul_f32_e32 v60, v61, v60
	v_med3_f32 v61, v63, s74, v170
	v_add_f32_e32 v63, 1.0, v64
	v_min_f32_e32 v64, 0x40e00000, v56
	v_mul_f32_e32 v56, 0x3fd9db23, v64
	v_mul_f32_e32 v56, 0xbfb8aa3b, v56
	v_rcp_f32_e32 v63, v63
	v_exp_f32_e32 v56, v56
	v_pk_add_f32 v[58:59], v[58:59], v[106:107]
	v_add_f32_e32 v61, 1.0, v61
	v_mul_f32_e32 v62, v62, v63
	v_add_f32_e32 v56, 1.0, v56
	v_min_f32_e32 v58, 0x40e00000, v58
	v_mul_f32_e32 v61, v61, v62
	v_rcp_f32_e32 v62, v56
	v_mul_f32_e32 v56, 0x3fd9db23, v58
	v_mul_f32_e32 v56, 0xbfb8aa3b, v56
	v_exp_f32_e32 v63, v56
	v_med3_f32 v57, v57, s74, v170
	v_pk_add_f32 v[52:53], v[52:53], v[92:93]
	v_cvt_pk_bf16_f32 v56, v60, v61
	v_mul_f32_e32 v60, v64, v62
	v_add_f32_e32 v57, 1.0, v57
	v_min_f32_e32 v52, 0x40e00000, v52
	v_add_f32_e32 v61, 1.0, v63
	v_mul_f32_e32 v57, v57, v60
	v_mul_f32_e32 v60, 0x3fd9db23, v52
	v_rcp_f32_e32 v61, v61
	v_mul_f32_e32 v60, 0xbfb8aa3b, v60
	v_exp_f32_e32 v62, v60
	v_med3_f32 v59, v59, s74, v170
	v_add_co_u32_e32 v60, vcc, s75, v154
	v_mul_f32_e32 v58, v58, v61
	v_add_f32_e32 v59, 1.0, v59
	v_addc_co_u32_e32 v61, vcc, 0, v155, vcc
	v_mul_f32_e32 v58, v59, v58
	v_cvt_pk_bf16_f32 v57, v57, v58
	global_store_dwordx2 v[60:61], v[56:57], off nt
	v_add_f32_e32 v56, 1.0, v62
	v_rcp_f32_e32 v56, v56
	v_pk_add_f32 v[54:55], v[54:55], v[94:95]
	v_med3_f32 v53, v53, s74, v170
	v_min_f32_e32 v54, 0x40e00000, v54
	v_mul_f32_e32 v52, v52, v56
	v_mul_f32_e32 v56, 0x3fd9db23, v54
	v_mul_f32_e32 v56, 0xbfb8aa3b, v56
	v_exp_f32_e32 v56, v56
	v_pk_add_f32 v[48:49], v[48:49], v[88:89]
	v_add_f32_e32 v53, 1.0, v53
	v_mul_f32_e32 v52, v53, v52
	v_med3_f32 v53, v55, s74, v170
	v_add_f32_e32 v55, 1.0, v56
	v_min_f32_e32 v56, 0x40e00000, v48
	v_mul_f32_e32 v48, 0x3fd9db23, v56
	v_mul_f32_e32 v48, 0xbfb8aa3b, v48
	v_rcp_f32_e32 v55, v55
	v_exp_f32_e32 v48, v48
	v_pk_add_f32 v[50:51], v[50:51], v[90:91]
	v_add_f32_e32 v53, 1.0, v53
	v_mul_f32_e32 v54, v54, v55
	v_add_f32_e32 v48, 1.0, v48
	v_min_f32_e32 v50, 0x40e00000, v50
	v_mul_f32_e32 v53, v53, v54
	v_rcp_f32_e32 v54, v48
	v_mul_f32_e32 v48, 0x3fd9db23, v50
	v_mul_f32_e32 v48, 0xbfb8aa3b, v48
	v_exp_f32_e32 v55, v48
	v_cvt_pk_bf16_f32 v48, v52, v53
	v_med3_f32 v51, v51, s74, v170
	v_pk_add_f32 v[44:45], v[44:45], v[108:109]
	v_add_f32_e32 v53, 1.0, v55
; __device__ __forceinline__ unsigned cvt_pk_bf16(float lo, float hi) { unsigned r; asm volatile("v_cvt_pk_bf16_f32 %0, %1, %2" : "=v"(r) : "v"(lo), "v"(hi)); return r; }
; __device__ __forceinline__ float sigm(float x) { return __builtin_amdgcn_rcpf(1.0f + __expf(-x)); }
; __device__ __forceinline__ float swiglu1(float g, float l) { g = fminf(g, 7.0f); l = fminf(fmaxf(l, -7.0f), 7.0f); return g * sigm(1.702f * g) * (l + 1.0f); }
;     __device__ __forceinline__ void operator()(const f32x4 (&acc)[2][2][4][2], const Unit& u, int wr, int wc, int fr, int fq) const {
;     ...
;             for (int m = 0; m < 4; ++m) { const int row = row0 + ai * HALF + m * 16;
; #pragma unroll
;                 for (int bj = 0; bj < 2; ++bj) { const f32x4 v0 = acc[ai][bj][m][0] + bv[bj][0], v1 = acc[ai][bj][m][1] + bv[bj][1];
;                     u32x2 w; w.x = cvt_pk_bf16(swiglu1(v0[0], v0[1]), swiglu1(v0[2], v0[3])); w.y = cvt_pk_bf16(swiglu1(v1[0], v1[1]), swiglu1(v1[2], v1[3]));
;                     *(u32x2*)(O + (size_t)row * 2048 + ((col0 + bj * HALF) >> 1)) = w; } }
	v_rcp_f32_e32 v53, v53
	v_add_f32_e32 v51, 1.0, v51
	v_min_f32_e32 v44, 0x40e00000, v44
	v_med3_f32 v49, v49, s74, v170
	v_mul_f32_e32 v50, v50, v53
	v_mul_f32_e32 v50, v51, v50
	v_mul_f32_e32 v51, 0x3fd9db23, v44
	v_mul_f32_e32 v51, 0xbfb8aa3b, v51
	v_exp_f32_e32 v51, v51
	v_mul_f32_e32 v52, v56, v54
	v_add_f32_e32 v49, 1.0, v49
	v_lshl_add_u64 v[58:59], v[154:155], 0, s[46:47]
	v_mul_f32_e32 v49, v49, v52
	v_cvt_pk_bf16_f32 v49, v49, v50
	global_store_dwordx2 v[58:59], v[48:49], off offset:128 nt
	v_add_f32_e32 v48, 1.0, v51
	v_rcp_f32_e32 v48, v48
	v_pk_add_f32 v[46:47], v[46:47], v[110:111]
	v_med3_f32 v45, v45, s74, v170
	v_min_f32_e32 v46, 0x40e00000, v46
	v_mul_f32_e32 v44, v44, v48
	v_mul_f32_e32 v48, 0x3fd9db23, v46
	v_mul_f32_e32 v48, 0xbfb8aa3b, v48
	v_exp_f32_e32 v48, v48
	v_pk_add_f32 v[32:33], v[32:33], v[104:105]
	v_add_f32_e32 v45, 1.0, v45
	v_mul_f32_e32 v44, v45, v44
	v_med3_f32 v45, v47, s74, v170
	v_add_f32_e32 v47, 1.0, v48
	v_min_f32_e32 v48, 0x40e00000, v32
	v_mul_f32_e32 v32, 0x3fd9db23, v48
	v_mul_f32_e32 v32, 0xbfb8aa3b, v32
	v_rcp_f32_e32 v47, v47
	v_exp_f32_e32 v32, v32
	v_pk_add_f32 v[34:35], v[34:35], v[106:107]
	v_add_f32_e32 v45, 1.0, v45
	v_mul_f32_e32 v46, v46, v47
	v_add_f32_e32 v32, 1.0, v32
	v_min_f32_e32 v34, 0x40e00000, v34
	v_mul_f32_e32 v45, v45, v46
	v_rcp_f32_e32 v46, v32
	v_mul_f32_e32 v32, 0x3fd9db23, v34
	v_mul_f32_e32 v32, 0xbfb8aa3b, v32
	v_exp_f32_e32 v47, v32
	v_cvt_pk_bf16_f32 v32, v44, v45
	v_med3_f32 v33, v33, s74, v170
	v_pk_add_f32 v[36:37], v[36:37], v[92:93]
	v_add_f32_e32 v45, 1.0, v47
	v_mul_f32_e32 v44, v48, v46
	v_rcp_f32_e32 v45, v45
	v_add_f32_e32 v33, 1.0, v33
	v_min_f32_e32 v36, 0x40e00000, v36
	v_mul_f32_e32 v33, v33, v44
	v_mul_f32_e32 v44, 0x3fd9db23, v36
	v_mul_f32_e32 v44, 0xbfb8aa3b, v44
	v_med3_f32 v35, v35, s74, v170
	v_exp_f32_e32 v46, v44
	v_mul_f32_e32 v34, v34, v45
	v_add_f32_e32 v35, 1.0, v35
	v_add_co_u32_e32 v44, vcc, s76, v154
	v_mul_f32_e32 v34, v35, v34
	v_cvt_pk_bf16_f32 v33, v33, v34
	s_nop 0
	v_addc_co_u32_e32 v45, vcc, 0, v155, vcc
	global_store_dwordx2 v[44:45], v[32:33], off nt
	v_pk_add_f32 v[32:33], v[38:39], v[94:95]
	v_add_f32_e32 v38, 1.0, v46
	v_min_f32_e32 v32, 0x40e00000, v32
	v_rcp_f32_e32 v44, v38
	v_pk_add_f32 v[38:39], v[42:43], v[90:91]
	v_mul_f32_e32 v42, 0x3fd9db23, v32
	v_mul_f32_e32 v42, 0xbfb8aa3b, v42
	v_exp_f32_e32 v42, v42
	v_med3_f32 v37, v37, s74, v170
	v_mul_f32_e32 v36, v36, v44
	v_add_f32_e32 v37, 1.0, v37
	v_mul_f32_e32 v36, v37, v36
	v_add_f32_e32 v37, 1.0, v42
	v_rcp_f32_e32 v37, v37
	v_pk_add_f32 v[40:41], v[40:41], v[88:89]
	v_med3_f32 v33, v33, s74, v170
	v_min_f32_e32 v40, 0x40e00000, v40
	v_mul_f32_e32 v42, 0x3fd9db23, v40
	v_mul_f32_e32 v42, 0xbfb8aa3b, v42
	v_mul_f32_e32 v32, v32, v37
	v_min_f32_e32 v37, 0x40e00000, v38
	v_exp_f32_e32 v42, v42
	v_mul_f32_e32 v38, 0x3fd9db23, v37
	v_mul_f32_e32 v38, 0xbfb8aa3b, v38
	v_exp_f32_e32 v38, v38
	v_add_f32_e32 v33, 1.0, v33
	v_mul_f32_e32 v32, v33, v32
	v_add_f32_e32 v33, 1.0, v42
	v_rcp_f32_e32 v33, v33
	v_add_f32_e32 v38, 1.0, v38
	v_rcp_f32_e32 v38, v38
	v_cvt_pk_bf16_f32 v32, v36, v32
	v_med3_f32 v36, v41, s74, v170
	v_mul_f32_e32 v33, v40, v33
	v_add_f32_e32 v36, 1.0, v36
	v_mul_f32_e32 v33, v36, v33
	v_med3_f32 v36, v39, s74, v170
	v_pk_add_f32 v[20:21], v[20:21], v[108:109]
	v_mul_f32_e32 v37, v37, v38
	v_add_f32_e32 v36, 1.0, v36
	v_min_f32_e32 v20, 0x40e00000, v20
	v_mul_f32_e32 v36, v36, v37
	v_mul_f32_e32 v37, 0x3fd9db23, v20
	v_mul_f32_e32 v37, 0xbfb8aa3b, v37
	v_exp_f32_e32 v37, v37
	v_lshl_add_u64 v[34:35], v[154:155], 0, s[48:49]
	v_cvt_pk_bf16_f32 v33, v33, v36
	global_store_dwordx2 v[34:35], v[32:33], off offset:128 nt
	v_add_f32_e32 v32, 1.0, v37
	v_rcp_f32_e32 v32, v32
	v_pk_add_f32 v[22:23], v[22:23], v[110:111]
	v_med3_f32 v21, v21, s74, v170
	v_min_f32_e32 v22, 0x40e00000, v22
	v_mul_f32_e32 v20, v20, v32
	v_mul_f32_e32 v32, 0x3fd9db23, v22
	v_mul_f32_e32 v32, 0xbfb8aa3b, v32
	v_exp_f32_e32 v32, v32
	v_pk_add_f32 v[16:17], v[16:17], v[104:105]
	v_add_f32_e32 v21, 1.0, v21
	v_mul_f32_e32 v20, v21, v20
	v_med3_f32 v21, v23, s74, v170
	v_add_f32_e32 v23, 1.0, v32
	v_min_f32_e32 v32, 0x40e00000, v16
	v_mul_f32_e32 v16, 0x3fd9db23, v32
	v_mul_f32_e32 v16, 0xbfb8aa3b, v16
	v_rcp_f32_e32 v23, v23
	v_exp_f32_e32 v16, v16
	v_pk_add_f32 v[18:19], v[18:19], v[106:107]
	v_add_f32_e32 v21, 1.0, v21
	v_mul_f32_e32 v22, v22, v23
	v_add_f32_e32 v16, 1.0, v16
	v_min_f32_e32 v18, 0x40e00000, v18
	v_mul_f32_e32 v21, v21, v22
	v_rcp_f32_e32 v22, v16
	v_mul_f32_e32 v16, 0x3fd9db23, v18
	v_mul_f32_e32 v16, 0xbfb8aa3b, v16
	v_exp_f32_e32 v23, v16
	v_cvt_pk_bf16_f32 v16, v20, v21
	v_med3_f32 v17, v17, s74, v170
	v_mul_f32_e32 v20, v32, v22
	v_add_f32_e32 v21, 1.0, v23
	v_rcp_f32_e32 v21, v21
	v_add_f32_e32 v17, 1.0, v17
	v_mul_f32_e32 v17, v17, v20
	v_med3_f32 v19, v19, s74, v170
	v_mul_f32_e32 v18, v18, v21
	v_pk_add_f32 v[20:21], v[24:25], v[92:93]
; __device__ __forceinline__ unsigned cvt_pk_bf16(float lo, float hi) { unsigned r; asm volatile("v_cvt_pk_bf16_f32 %0, %1, %2" : "=v"(r) : "v"(lo), "v"(hi)); return r; }
; __device__ __forceinline__ float sigm(float x) { return __builtin_amdgcn_rcpf(1.0f + __expf(-x)); }
; __device__ __forceinline__ float swiglu1(float g, float l) { g = fminf(g, 7.0f); l = fminf(fmaxf(l, -7.0f), 7.0f); return g * sigm(1.702f * g) * (l + 1.0f); }
;     __device__ __forceinline__ void operator()(const f32x4 (&acc)[2][2][4][2], const Unit& u, int wr, int wc, int fr, int fq) const {
;     ...
;             for (int m = 0; m < 4; ++m) { const int row = row0 + ai * HALF + m * 16;
; #pragma unroll
;                 for (int bj = 0; bj < 2; ++bj) { const f32x4 v0 = acc[ai][bj][m][0] + bv[bj][0], v1 = acc[ai][bj][m][1] + bv[bj][1];
;                     u32x2 w; w.x = cvt_pk_bf16(swiglu1(v0[0], v0[1]), swiglu1(v0[2], v0[3])); w.y = cvt_pk_bf16(swiglu1(v1[0], v1[1]), swiglu1(v1[2], v1[3]));
;                     *(u32x2*)(O + (size_t)row * 2048 + ((col0 + bj * HALF) >> 1)) = w; } }
	v_add_f32_e32 v19, 1.0, v19
	v_min_f32_e32 v20, 0x40e00000, v20
	v_mul_f32_e32 v22, 0x3fd9db23, v20
	v_mul_f32_e32 v22, 0xbfb8aa3b, v22
	v_exp_f32_e32 v24, v22
	v_add_co_u32_e32 v22, vcc, s77, v154
	v_mul_f32_e32 v18, v19, v18
	s_nop 0
	v_addc_co_u32_e32 v23, vcc, 0, v155, vcc
	v_cvt_pk_bf16_f32 v17, v17, v18
	global_store_dwordx2 v[22:23], v[16:17], off nt
	v_add_f32_e32 v22, 1.0, v24
	v_pk_add_f32 v[16:17], v[26:27], v[94:95]
	v_rcp_f32_e32 v26, v22
	v_min_f32_e32 v16, 0x40e00000, v16
	v_med3_f32 v21, v21, s74, v170
	v_add_f32_e32 v21, 1.0, v21
	v_mul_f32_e32 v20, v20, v26
	v_mul_f32_e32 v26, 0x3fd9db23, v16
	v_mul_f32_e32 v26, 0xbfb8aa3b, v26
	v_exp_f32_e32 v26, v26
	v_mul_f32_e32 v20, v21, v20
	v_pk_add_f32 v[24:25], v[28:29], v[88:89]
	v_pk_add_f32 v[22:23], v[30:31], v[90:91]
	v_add_f32_e32 v21, 1.0, v26
	v_rcp_f32_e32 v21, v21
	v_min_f32_e32 v24, 0x40e00000, v24
	v_mul_f32_e32 v26, 0x3fd9db23, v24
	v_mul_f32_e32 v26, 0xbfb8aa3b, v26
	v_mul_f32_e32 v16, v16, v21
	v_min_f32_e32 v21, 0x40e00000, v22
	v_exp_f32_e32 v26, v26
	v_mul_f32_e32 v22, 0x3fd9db23, v21
	v_mul_f32_e32 v22, 0xbfb8aa3b, v22
	v_med3_f32 v17, v17, s74, v170
	v_exp_f32_e32 v22, v22
	v_add_f32_e32 v17, 1.0, v17
	v_mul_f32_e32 v16, v17, v16
	v_add_f32_e32 v17, 1.0, v26
	v_rcp_f32_e32 v17, v17
	v_add_f32_e32 v22, 1.0, v22
	v_rcp_f32_e32 v22, v22
	v_cvt_pk_bf16_f32 v16, v20, v16
	v_med3_f32 v20, v25, s74, v170
	v_mul_f32_e32 v17, v24, v17
	v_add_f32_e32 v20, 1.0, v20
	v_mul_f32_e32 v17, v20, v17
	v_med3_f32 v20, v23, s74, v170
	v_pk_add_f32 v[4:5], v[4:5], v[108:109]
	v_mul_f32_e32 v21, v21, v22
	v_add_f32_e32 v20, 1.0, v20
	v_min_f32_e32 v4, 0x40e00000, v4
	v_mul_f32_e32 v20, v20, v21
	v_mul_f32_e32 v21, 0x3fd9db23, v4
	v_mul_f32_e32 v21, 0xbfb8aa3b, v21
	v_exp_f32_e32 v21, v21
	v_lshl_add_u64 v[18:19], v[154:155], 0, s[50:51]
	v_cvt_pk_bf16_f32 v17, v17, v20
	global_store_dwordx2 v[18:19], v[16:17], off offset:128 nt
	v_add_f32_e32 v16, 1.0, v21
	v_rcp_f32_e32 v16, v16
	v_pk_add_f32 v[6:7], v[6:7], v[110:111]
	v_med3_f32 v5, v5, s74, v170
	v_min_f32_e32 v6, 0x40e00000, v6
	v_mul_f32_e32 v4, v4, v16
	v_mul_f32_e32 v16, 0x3fd9db23, v6
	v_mul_f32_e32 v16, 0xbfb8aa3b, v16
	v_exp_f32_e32 v16, v16
	v_pk_add_f32 v[0:1], v[0:1], v[104:105]
	v_add_f32_e32 v5, 1.0, v5
	v_mul_f32_e32 v4, v5, v4
	v_med3_f32 v5, v7, s74, v170
	v_add_f32_e32 v7, 1.0, v16
	v_min_f32_e32 v16, 0x40e00000, v0
	v_mul_f32_e32 v0, 0x3fd9db23, v16
	v_mul_f32_e32 v0, 0xbfb8aa3b, v0
	v_rcp_f32_e32 v7, v7
	v_exp_f32_e32 v0, v0
	v_pk_add_f32 v[2:3], v[2:3], v[106:107]
	v_add_f32_e32 v5, 1.0, v5
	v_mul_f32_e32 v6, v6, v7
	v_add_f32_e32 v0, 1.0, v0
	v_min_f32_e32 v2, 0x40e00000, v2
	v_mul_f32_e32 v5, v5, v6
	v_rcp_f32_e32 v6, v0
	v_mul_f32_e32 v0, 0x3fd9db23, v2
	v_mul_f32_e32 v0, 0xbfb8aa3b, v0
	v_exp_f32_e32 v7, v0
	v_cvt_pk_bf16_f32 v0, v4, v5
	v_med3_f32 v1, v1, s74, v170
	v_mul_f32_e32 v4, v16, v6
	v_add_f32_e32 v5, 1.0, v7
	v_rcp_f32_e32 v5, v5
	v_add_f32_e32 v1, 1.0, v1
	v_mul_f32_e32 v1, v1, v4
	v_med3_f32 v3, v3, s74, v170
	v_mul_f32_e32 v2, v2, v5
	v_pk_add_f32 v[4:5], v[8:9], v[92:93]
	v_add_f32_e32 v3, 1.0, v3
	v_min_f32_e32 v4, 0x40e00000, v4
	v_mul_f32_e32 v6, 0x3fd9db23, v4
	v_mul_f32_e32 v6, 0xbfb8aa3b, v6
	v_exp_f32_e32 v8, v6
	v_add_co_u32_e32 v6, vcc, s78, v154
	v_mul_f32_e32 v2, v3, v2
	s_nop 0
	v_addc_co_u32_e32 v7, vcc, 0, v155, vcc
	v_cvt_pk_bf16_f32 v1, v1, v2
	global_store_dwordx2 v[6:7], v[0:1], off nt
	v_add_f32_e32 v6, 1.0, v8
	v_pk_add_f32 v[0:1], v[10:11], v[94:95]
	v_rcp_f32_e32 v10, v6
	v_min_f32_e32 v0, 0x40e00000, v0
	v_med3_f32 v5, v5, s74, v170
	v_add_f32_e32 v5, 1.0, v5
	v_mul_f32_e32 v4, v4, v10
	v_mul_f32_e32 v10, 0x3fd9db23, v0
	v_mul_f32_e32 v10, 0xbfb8aa3b, v10
	v_exp_f32_e32 v10, v10
	v_mul_f32_e32 v4, v5, v4
	v_pk_add_f32 v[8:9], v[12:13], v[88:89]
	v_pk_add_f32 v[6:7], v[14:15], v[90:91]
	v_add_f32_e32 v5, 1.0, v10
	v_rcp_f32_e32 v5, v5
	v_min_f32_e32 v8, 0x40e00000, v8
	v_mul_f32_e32 v10, 0x3fd9db23, v8
	v_mul_f32_e32 v10, 0xbfb8aa3b, v10
	v_mul_f32_e32 v0, v0, v5
	v_min_f32_e32 v5, 0x40e00000, v6
	v_exp_f32_e32 v10, v10
	v_mul_f32_e32 v6, 0x3fd9db23, v5
	v_mul_f32_e32 v6, 0xbfb8aa3b, v6
	v_med3_f32 v1, v1, s74, v170
	v_exp_f32_e32 v6, v6
	v_add_f32_e32 v1, 1.0, v1
	v_mul_f32_e32 v0, v1, v0
	v_add_f32_e32 v1, 1.0, v10
	v_rcp_f32_e32 v1, v1
	v_add_f32_e32 v6, 1.0, v6
	v_rcp_f32_e32 v6, v6
	v_cvt_pk_bf16_f32 v0, v4, v0
	v_med3_f32 v4, v9, s74, v170
	v_mul_f32_e32 v1, v8, v1
	v_add_f32_e32 v4, 1.0, v4
	v_mul_f32_e32 v1, v4, v1
	v_med3_f32 v4, v7, s74, v170
	v_lshl_add_u64 v[2:3], v[154:155], 0, s[52:53]
	v_mul_f32_e32 v5, v5, v6
	v_add_f32_e32 v4, 1.0, v4
	s_and_b64 vcc, exec, s[2:3]
	s_mov_b64 s[2:3], -1
	v_mul_f32_e32 v4, v4, v5
	v_cvt_pk_bf16_f32 v1, v1, v4
	global_store_dwordx2 v[2:3], v[0:1], off offset:128 nt
	s_cbranch_vccnz .LBB0_2293
	s_andn2_b64 vcc, exec, s[30:31]
	s_cbranch_vccnz .LBB0_2292
	s_barrier
	s_branch .LBB0_2292

;     __device__ __forceinline__ void operator()(const f32x4 (&acc)[2][2][4][2], const Unit& u, int wr, int wc, int fr, int fq) const {
;         const int row0 = u.pm * BM + wr * 64 + fr, col0 = u.pn * BM + wc * 32 + 8 * fq; const float* bb = bias + (size_t)u.e * 2048;
;         f32x4 bv[2][2];
; #pragma unroll
;         for (int bj = 0; bj < 2; ++bj)
; #pragma unroll
;             for (int n = 0; n < 2; ++n) bv[bj][n] = *(const f32x4*)(bb + col0 + bj * HALF + 4 * n);
; #pragma unroll
;         for (int ai = 0; ai < 2; ++ai)
; #pragma unroll
;             for (int m = 0; m < 4; ++m) { const int row = row0 + ai * HALF + m * 16;
.LBB0_3498:
	v_ashrrev_i32_e32 v129, 31, v128
	v_lshl_or_b32 v162, s54, 8, v166
	v_lshlrev_b64 v[128:129], 13, v[128:129]
	v_lshl_add_u64 v[128:129], s[10:11], 0, v[128:129]
	v_ashrrev_i32_e32 v163, 31, v162
	v_lshl_add_u64 v[128:129], v[162:163], 2, v[128:129]
	global_load_dwordx4 v[140:143], v[128:129], off
	global_load_dwordx4 v[136:139], v[128:129], off offset:16
	global_load_dwordx4 v[132:135], v[128:129], off offset:512
	s_nop 0
	global_load_dwordx4 v[128:131], v[128:129], off offset:528
	v_lshl_add_u32 v170, s52, 8, v164
	v_ashrrev_i32_e32 v171, 31, v170
	v_or_b32_e32 v172, 16, v170
	v_or_b32_e32 v174, 32, v170
	v_or_b32_e32 v176, 48, v170
	v_lshlrev_b64 v[170:171], 12, v[170:171]
	v_lshlrev_b64 v[178:179], 1, v[162:163]
	v_ashrrev_i32_e32 v173, 31, v172
	v_lshl_add_u64 v[162:163], s[8:9], 0, v[170:171]
	v_ashrrev_i32_e32 v175, 31, v174
	v_ashrrev_i32_e32 v177, 31, v176
	v_lshlrev_b64 v[170:171], 12, v[172:173]
	v_lshl_add_u64 v[162:163], v[162:163], 0, v[178:179]
	v_lshlrev_b64 v[172:173], 12, v[174:175]
	v_lshlrev_b64 v[174:175], 12, v[176:177]
	v_lshl_add_u64 v[170:171], s[8:9], 0, v[170:171]
	v_lshl_add_u64 v[170:171], v[170:171], 0, v[178:179]
	v_lshl_add_u64 v[172:173], s[8:9], 0, v[172:173]
	v_lshl_add_u64 v[172:173], v[172:173], 0, v[178:179]
	v_lshl_add_u64 v[174:175], s[8:9], 0, v[174:175]
	s_waitcnt vmcnt(0)
; __device__ __forceinline__ unsigned cvt_pk_bf16(float lo, float hi) { unsigned r; asm volatile("v_cvt_pk_bf16_f32 %0, %1, %2" : "=v"(r) : "v"(lo), "v"(hi)); return r; }
;     __device__ __forceinline__ void operator()(const f32x4 (&acc)[2][2][4][2], const Unit& u, int wr, int wc, int fr, int fq) const {
;     ...
;             for (int m = 0; m < 4; ++m) { const int row = row0 + ai * HALF + m * 16;
; #pragma unroll
;                 for (int bj = 0; bj < 2; ++bj) { const f32x4 v0 = acc[ai][bj][m][0] + bv[bj][0], v1 = acc[ai][bj][m][1] + bv[bj][1];
;                     u32x4 w; w.x = cvt_pk_bf16(v0[0], v0[1]); w.y = cvt_pk_bf16(v0[2], v0[3]); w.z = cvt_pk_bf16(v1[0], v1[1]); w.w = cvt_pk_bf16(v1[2], v1[3]);
;                     *(u32x4*)(O + (size_t)row * 2048 + col0 + bj * HALF) = w; } }
	v_pk_add_f32 v[126:127], v[126:127], v[142:143]
	v_pk_add_f32 v[124:125], v[124:125], v[140:141]
	v_pk_add_f32 v[122:123], v[122:123], v[138:139]
	v_pk_add_f32 v[180:181], v[72:73], v[128:129]
	v_cvt_pk_bf16_f32 v72, v124, v125
	v_cvt_pk_bf16_f32 v73, v126, v127
	v_pk_add_f32 v[120:121], v[120:121], v[136:137]
	v_pk_add_f32 v[106:107], v[106:107], v[134:135]
	v_pk_add_f32 v[104:105], v[104:105], v[132:133]
	v_pk_add_f32 v[176:177], v[74:75], v[130:131]
	v_cvt_pk_bf16_f32 v74, v120, v121
	v_cvt_pk_bf16_f32 v75, v122, v123
	global_store_dwordx4 v[162:163], v[72:75], off nt
	v_pk_add_f32 v[98:99], v[98:99], v[130:131]
	v_pk_add_f32 v[96:97], v[96:97], v[128:129]
	v_cvt_pk_bf16_f32 v72, v104, v105
	v_cvt_pk_bf16_f32 v73, v106, v107
	v_pk_add_f32 v[118:119], v[118:119], v[142:143]
	v_pk_add_f32 v[116:117], v[116:117], v[140:141]
	v_cvt_pk_bf16_f32 v74, v96, v97
	v_cvt_pk_bf16_f32 v75, v98, v99
	global_store_dwordx4 v[162:163], v[72:75], off offset:256 nt
	v_pk_add_f32 v[114:115], v[114:115], v[138:139]
	v_pk_add_f32 v[112:113], v[112:113], v[136:137]
	v_cvt_pk_bf16_f32 v72, v116, v117
	v_cvt_pk_bf16_f32 v73, v118, v119
	v_pk_add_f32 v[90:91], v[90:91], v[134:135]
	v_pk_add_f32 v[88:89], v[88:89], v[132:133]
	v_cvt_pk_bf16_f32 v74, v112, v113
	v_cvt_pk_bf16_f32 v75, v114, v115
	global_store_dwordx4 v[170:171], v[72:75], off nt
	v_pk_add_f32 v[82:83], v[82:83], v[130:131]
	v_pk_add_f32 v[80:81], v[80:81], v[128:129]
	v_cvt_pk_bf16_f32 v72, v88, v89
	v_cvt_pk_bf16_f32 v73, v90, v91
	v_pk_add_f32 v[110:111], v[110:111], v[142:143]
	v_pk_add_f32 v[108:109], v[108:109], v[140:141]
	v_cvt_pk_bf16_f32 v74, v80, v81
	v_cvt_pk_bf16_f32 v75, v82, v83
	global_store_dwordx4 v[170:171], v[72:75], off offset:256 nt
	v_pk_add_f32 v[102:103], v[102:103], v[138:139]
	v_pk_add_f32 v[100:101], v[100:101], v[136:137]
	v_cvt_pk_bf16_f32 v72, v108, v109
	v_cvt_pk_bf16_f32 v73, v110, v111
	v_pk_add_f32 v[78:79], v[78:79], v[134:135]
	v_pk_add_f32 v[76:77], v[76:77], v[132:133]
	v_cvt_pk_bf16_f32 v74, v100, v101
	v_cvt_pk_bf16_f32 v75, v102, v103
	global_store_dwordx4 v[172:173], v[72:75], off nt
	v_pk_add_f32 v[94:95], v[94:95], v[142:143]
	v_pk_add_f32 v[92:93], v[92:93], v[140:141]
	v_cvt_pk_bf16_f32 v72, v76, v77
	v_cvt_pk_bf16_f32 v73, v78, v79
	v_cvt_pk_bf16_f32 v74, v180, v181
	v_cvt_pk_bf16_f32 v75, v176, v177
	global_store_dwordx4 v[172:173], v[72:75], off offset:256 nt
	v_lshl_add_u64 v[76:77], v[174:175], 0, v[178:179]
	v_pk_add_f32 v[86:87], v[86:87], v[138:139]
	v_cvt_pk_bf16_f32 v72, v92, v93
	v_cvt_pk_bf16_f32 v73, v94, v95
	v_pk_add_f32 v[84:85], v[84:85], v[136:137]
	v_pk_add_f32 v[70:71], v[70:71], v[134:135]
	v_cvt_pk_bf16_f32 v74, v84, v85
	v_cvt_pk_bf16_f32 v75, v86, v87
	global_store_dwordx4 v[76:77], v[72:75], off nt
	v_pk_add_f32 v[68:69], v[68:69], v[132:133]
	v_pk_add_f32 v[62:63], v[62:63], v[142:143]
	v_pk_add_f32 v[72:73], v[66:67], v[130:131]
	v_pk_add_f32 v[66:67], v[64:65], v[128:129]
	v_cvt_pk_bf16_f32 v64, v68, v69
	v_cvt_pk_bf16_f32 v65, v70, v71
	v_pk_add_f32 v[60:61], v[60:61], v[140:141]
	v_cvt_pk_bf16_f32 v66, v66, v67
	v_cvt_pk_bf16_f32 v67, v72, v73
	global_store_dwordx4 v[76:77], v[64:67], off offset:256 nt
	v_pk_add_f32 v[54:55], v[54:55], v[134:135]
	v_pk_add_f32 v[52:53], v[52:53], v[132:133]
	v_pk_add_f32 v[64:65], v[58:59], v[138:139]
	v_pk_add_f32 v[58:59], v[56:57], v[136:137]
	v_cvt_pk_bf16_f32 v56, v60, v61
	v_cvt_pk_bf16_f32 v57, v62, v63
	v_add_co_u32_e32 v62, vcc, s70, v162
	v_cvt_pk_bf16_f32 v58, v58, v59
	v_cvt_pk_bf16_f32 v59, v64, v65
	v_lshl_add_u64 v[60:61], v[162:163], 0, s[14:15]
	s_nop 0
	v_addc_co_u32_e32 v63, vcc, 0, v163, vcc
	global_store_dwordx4 v[62:63], v[56:59], off nt
	v_pk_add_f32 v[38:39], v[38:39], v[134:135]
	v_pk_add_f32 v[36:37], v[36:37], v[132:133]
	v_pk_add_f32 v[56:57], v[46:47], v[130:131]
	v_pk_add_f32 v[46:47], v[44:45], v[128:129]
	v_cvt_pk_bf16_f32 v44, v52, v53
	v_cvt_pk_bf16_f32 v45, v54, v55
	v_pk_add_f32 v[22:23], v[22:23], v[134:135]
	v_cvt_pk_bf16_f32 v46, v46, v47
	v_cvt_pk_bf16_f32 v47, v56, v57
	global_store_dwordx4 v[60:61], v[44:47], off offset:256 nt
	v_pk_add_f32 v[20:21], v[20:21], v[132:133]
	v_pk_add_f32 v[6:7], v[6:7], v[134:135]
	v_pk_add_f32 v[46:47], v[48:49], v[140:141]
	v_pk_add_f32 v[48:49], v[42:43], v[138:139]
	v_pk_add_f32 v[42:43], v[40:41], v[136:137]
	v_cvt_pk_bf16_f32 v40, v46, v47
	v_add_co_u32_e32 v46, vcc, s71, v162
	v_pk_add_f32 v[44:45], v[50:51], v[142:143]
	s_nop 0
	v_addc_co_u32_e32 v47, vcc, 0, v163, vcc
	v_cvt_pk_bf16_f32 v41, v44, v45
	v_cvt_pk_bf16_f32 v42, v42, v43
	v_cvt_pk_bf16_f32 v43, v48, v49
	global_store_dwordx4 v[46:47], v[40:43], off nt
	v_lshl_add_u64 v[44:45], v[162:163], 0, s[38:39]
	v_pk_add_f32 v[4:5], v[4:5], v[132:133]
	v_pk_add_f32 v[40:41], v[30:31], v[130:131]
	v_pk_add_f32 v[30:31], v[28:29], v[128:129]
	v_cvt_pk_bf16_f32 v28, v36, v37
	v_cvt_pk_bf16_f32 v29, v38, v39
	s_nop 0
	v_cvt_pk_bf16_f32 v30, v30, v31
	v_cvt_pk_bf16_f32 v31, v40, v41
	global_store_dwordx4 v[44:45], v[28:31], off offset:256 nt
	s_nop 1
	v_pk_add_f32 v[30:31], v[32:33], v[140:141]
	v_pk_add_f32 v[32:33], v[26:27], v[138:139]
	v_pk_add_f32 v[26:27], v[24:25], v[136:137]
	v_cvt_pk_bf16_f32 v24, v30, v31
	v_add_co_u32_e32 v30, vcc, s72, v162
	v_pk_add_f32 v[28:29], v[34:35], v[142:143]
	s_nop 0
	v_addc_co_u32_e32 v31, vcc, 0, v163, vcc
	v_cvt_pk_bf16_f32 v25, v28, v29
	v_cvt_pk_bf16_f32 v26, v26, v27
	v_cvt_pk_bf16_f32 v27, v32, v33
	global_store_dwordx4 v[30:31], v[24:27], off nt
	v_lshl_add_u64 v[28:29], v[162:163], 0, s[40:41]
	s_nop 0
	v_pk_add_f32 v[24:25], v[14:15], v[130:131]
	v_pk_add_f32 v[14:15], v[12:13], v[128:129]
	v_cvt_pk_bf16_f32 v12, v20, v21
	v_cvt_pk_bf16_f32 v13, v22, v23
	s_nop 0
	v_cvt_pk_bf16_f32 v14, v14, v15
	v_cvt_pk_bf16_f32 v15, v24, v25
	global_store_dwordx4 v[28:29], v[12:15], off offset:256 nt
	s_nop 1
	v_pk_add_f32 v[14:15], v[16:17], v[140:141]
	v_pk_add_f32 v[16:17], v[10:11], v[138:139]
	v_pk_add_f32 v[10:11], v[8:9], v[136:137]
	v_cvt_pk_bf16_f32 v8, v14, v15
	v_add_co_u32_e32 v14, vcc, s73, v162
	v_pk_add_f32 v[12:13], v[18:19], v[142:143]
	s_nop 0
	v_addc_co_u32_e32 v15, vcc, 0, v163, vcc
	v_cvt_pk_bf16_f32 v9, v12, v13
	v_cvt_pk_bf16_f32 v10, v10, v11
	v_cvt_pk_bf16_f32 v11, v16, v17
	v_lshl_add_u64 v[12:13], v[162:163], 0, s[42:43]
	global_store_dwordx4 v[14:15], v[8:11], off nt
	s_andn2_b64 vcc, exec, s[48:49]
	s_mov_b64 s[48:49], -1
	v_pk_add_f32 v[8:9], v[2:3], v[130:131]
	v_pk_add_f32 v[2:3], v[0:1], v[128:129]
	v_cvt_pk_bf16_f32 v0, v4, v5
	v_cvt_pk_bf16_f32 v1, v6, v7
	s_nop 0
	v_cvt_pk_bf16_f32 v2, v2, v3
	v_cvt_pk_bf16_f32 v3, v8, v9
	global_store_dwordx4 v[12:13], v[0:3], off offset:256 nt
	s_cbranch_vccnz .LBB0_3490
	s_andn2_b64 vcc, exec, s[12:13]
	s_cbranch_vccnz .LBB0_3489
	s_barrier
	s_branch .LBB0_3489
